# support side: expert-weight conversion takes 32 items (16 tickets) per atomic grab instead of 16, halving the per-chunk pipeline drain; attention as v50
# speedup vs baseline: 1.0034x; 1.0034x over previous
; #define LAS __attribute__((address_space(3)))
; __device__ __forceinline__ int otid() { int t = threadIdx.x; asm volatile("" : "+v"(t)); return t; }
; __global__ void __launch_bounds__(512, 2) mk_fwd(Params p_unused) {
;     ...
;         {
;             const int tid = otid(), lane = tid & 63, wave = __builtin_amdgcn_readfirstlane(tid >> 6);
;             LAS float* scr = (LAS float*)(L + wave * 16384);
;             unsigned* qc = WSP(unsigned, WS_CTL) + CW_Q;
;             constexpr int I_G = (DM / 64) * (DE / 32), I_D = (DE / 64) * (DM / 32), PER = 2 * I_G + I_D; constexpr unsigned NTICK = 64u * PER / 2u;
;             auto decode = [&](int it) { TItem d; const int le = it / PER; int r = it - le * PER;
;                 if (r < I_G) { d.W = kp->w_gate + (size_t)le * DM * DE; d.WT = WSP(bf16_t, WS_WGU) + (size_t)le * 2048 * DM; d.K = DM; d.N = DE; d.kind = 1; }
;                 else if ((r -= I_G) < I_G) { d.W = kp->w_up + (size_t)le * DM * DE; d.WT = WSP(bf16_t, WS_WGU) + (size_t)le * 2048 * DM; d.K = DM; d.N = DE; d.kind = 2; }
;                 else { r -= I_G; d.W = kp->w_down + (size_t)le * DE * DM; d.WT = WSP(bf16_t, WS_WD) + (size_t)le * DM * DE; d.K = DE; d.N = DM; d.kind = 0; }
;                 const int nblk = d.N / 32; d.k0 = 64 * (r / nblk); d.n0 = 32 * (r % nblk); return d; };
;             static_assert(NTICK % 8u == 0u, "ticket chunks");
;             auto grab = [&]() { unsigned t = 0; if (lane == 0) t = __hip_atomic_fetch_add(qc, 8u, __ATOMIC_RELAXED, __HIP_MEMORY_SCOPE_AGENT); return (unsigned)__builtin_amdgcn_readfirstlane((int)t); };
;             for (unsigned tb = grab(); tb < NTICK; tb = grab()) {
.LBB0_468:
	s_load_dwordx2 s[42:43], s[30:31], 0x80
	s_load_dwordx2 s[44:45], s[30:31], 0x88
	s_load_dwordx2 s[46:47], s[30:31], 0x90
	s_add_u32 s4, s28, 0x3000
	s_addc_u32 s5, s29, 0
	s_add_u32 s36, s28, 0x21800000
	s_addc_u32 s37, s29, 0
	s_add_u32 s38, s28, 0x1800000
	s_addc_u32 s39, s29, 0
	v_and_b32_e32 v1, 63, v0
	v_lshrrev_b32_e32 v2, 3, v1
	v_and_b32_e32 v3, 7, v1
	v_lshlrev_b32_e32 v4, 4, v3
	v_lshlrev_b32_e32 v5, 4, v2
	v_lshl_or_b32 v10, v2, 15, v4
	v_lshl_or_b32 v18, v2, 16, v4
	v_lshl_or_b32 v26, v3, 14, v5
	v_lshl_or_b32 v30, v3, 13, v5
	v_add_u32_e32 v11, 0x1000, v10
	v_add_u32_e32 v19, 0x2000, v18
	v_add_u32_e32 v12, 0x2000, v10
	v_add_u32_e32 v20, 0x4000, v18
	v_add_u32_e32 v13, 0x3000, v10
	v_add_u32_e32 v21, 0x6000, v18
	v_add_u32_e32 v14, 0x4000, v10
	v_add_u32_e32 v22, 0x8000, v18
	v_add_u32_e32 v15, 0x5000, v10
	v_add_u32_e32 v23, 0xa000, v18
	v_add_u32_e32 v16, 0x6000, v10
	v_add_u32_e32 v24, 0xc000, v18
	v_add_u32_e32 v17, 0x7000, v10
	v_add_u32_e32 v25, 0xe000, v18
	v_add_u32_e32 v27, 0x1000, v26
	v_add_u32_e32 v31, 0x800, v30
	v_add_u32_e32 v28, 0x2000, v26
	v_add_u32_e32 v32, 0x1000, v30
	v_add_u32_e32 v29, 0x3000, v26
	v_add_u32_e32 v33, 0x1800, v30
	v_mov_b32_e32 v9, 0
	v_mov_b32_e32 v8, 16
	s_waitcnt lgkmcnt(0)
	s_mov_b64 exec, 1
	global_atomic_add v7, v9, v8, s[4:5] sc0
	s_mov_b64 exec, -1
	s_waitcnt vmcnt(0)
	v_readfirstlane_b32 s40, v7
	s_nop 3

; #define GAS __attribute__((address_space(1)))
; #define LAS __attribute__((address_space(3)))
; #define LDS_WAIT() asm volatile("s_waitcnt lgkmcnt(0)" ::: "memory")
; __device__ __forceinline__ unsigned pk2(float lo, float hi) { unsigned r; asm("v_cvt_pk_bf16_f32 %0, %1, %2" : "=v"(r) : "v"(lo), "v"(hi)); return r; }
; __device__ __forceinline__ void t_load(const TItem& d, f32x4 (&r)[8], int lane) {
;     const float* p = d.W + (size_t)(d.k0 + (lane >> 3)) * d.N + d.n0 + (lane & 7) * 4;
; #pragma unroll
;     for (int i = 0; i < 8; ++i) r[i] = __builtin_nontemporal_load((const f32x4*)(p + (size_t)(8 * i) * d.N));
; }
; __device__ __forceinline__ void t_store(const TItem& d, const f32x4 (&r)[8], LAS float* scr, int lane) {
; #pragma unroll
;     for (int i = 0; i < 8; ++i) *(LAS f32x4*)(scr + (8 * i + (lane >> 3)) * 32 + (((lane & 7) * 4 + 8 * i) & 31)) = r[i];
;     LDS_WAIT(); asm volatile("" ::: "memory");
;     const int c = lane >> 3, nl = lane & 7;
; #pragma unroll
;     for (int j = 0; j < 4; ++j) { const int n = nl + 8 * j; const LAS float* s = scr + (8 * c) * 32 + ((n + 8 * c) & 31);
;         v4u o; o.x = pk2(s[0 * 32], s[1 * 32]); o.y = pk2(s[2 * 32], s[3 * 32]); o.z = pk2(s[4 * 32], s[5 * 32]); o.w = pk2(s[6 * 32], s[7 * 32]);
;         __builtin_nontemporal_store(o, (GAS v4u*)(d.WT + (size_t)t_drow(d.kind, d.n0 + n) * d.K + d.k0 + 8 * c)); }
;     LDS_WAIT(); asm volatile("" ::: "memory");
; }
; __global__ void __launch_bounds__(512, 2) mk_fwd(Params p_unused) {
;     ...
;             for (unsigned tb = grab(); tb < NTICK; tb = grab()) {
;                 TItem a0 = decode((int)(2u * tb)); TItem a1 = a0; a1.n0 += 32;
;                 f32x4 ra[8], rb[8], rc[8], rd[8]; t_load(a0, ra, lane); t_load(a1, rb, lane);
;                 _Pragma("unroll 1") for (unsigned u = 0; u < 8u; u += 2u) {
;                     const TItem b0 = decode((int)(2u * (tb + u + 1u))); TItem b1 = b0; b1.n0 += 32;
;                     t_load(b0, rc, lane); t_load(b1, rd, lane);
;                     t_store(a0, ra, scr, lane); t_store(a1, rb, scr, lane);
;                     if (u + 2u < 8u) { a0 = decode((int)(2u * (tb + u + 2u))); a1 = a0; a1.n0 += 32; t_load(a0, ra, lane); t_load(a1, rb, lane); }
;                     t_store(b0, rc, scr, lane); t_store(b1, rd, scr, lane);
;                 }
.Lcv_go:
	global_load_dwordx4 v[54:57], v34, s[8:9] offset:0 nt
	global_load_dwordx4 v[58:61], v35, s[8:9] offset:0 nt
	global_load_dwordx4 v[62:65], v36, s[8:9] offset:0 nt
	global_load_dwordx4 v[66:69], v37, s[8:9] offset:0 nt
	global_load_dwordx4 v[70:73], v38, s[8:9] offset:0 nt
	global_load_dwordx4 v[74:77], v39, s[8:9] offset:0 nt
	global_load_dwordx4 v[78:81], v40, s[8:9] offset:0 nt
	global_load_dwordx4 v[82:85], v41, s[8:9] offset:0 nt
	global_load_dwordx4 v[86:89], v34, s[8:9] offset:128 nt
	global_load_dwordx4 v[90:93], v35, s[8:9] offset:128 nt
	global_load_dwordx4 v[94:97], v36, s[8:9] offset:128 nt
	global_load_dwordx4 v[98:101], v37, s[8:9] offset:128 nt
	global_load_dwordx4 v[102:105], v38, s[8:9] offset:128 nt
	global_load_dwordx4 v[106:109], v39, s[8:9] offset:128 nt
	global_load_dwordx4 v[110:113], v40, s[8:9] offset:128 nt
	global_load_dwordx4 v[114:117], v41, s[8:9] offset:128 nt
	global_load_dwordx4 v[118:121], v34, s[8:9] offset:256 nt
	global_load_dwordx4 v[122:125], v35, s[8:9] offset:256 nt
	global_load_dwordx4 v[126:129], v36, s[8:9] offset:256 nt
	global_load_dwordx4 v[130:133], v37, s[8:9] offset:256 nt
	global_load_dwordx4 v[134:137], v38, s[8:9] offset:256 nt
	global_load_dwordx4 v[138:141], v39, s[8:9] offset:256 nt
	global_load_dwordx4 v[142:145], v40, s[8:9] offset:256 nt
	global_load_dwordx4 v[146:149], v41, s[8:9] offset:256 nt
	global_load_dwordx4 v[166:169], v34, s[8:9] offset:384 nt
	global_load_dwordx4 v[170:173], v35, s[8:9] offset:384 nt
	global_load_dwordx4 v[174:177], v36, s[8:9] offset:384 nt
	global_load_dwordx4 v[178:181], v37, s[8:9] offset:384 nt
	global_load_dwordx4 v[182:185], v38, s[8:9] offset:384 nt
	global_load_dwordx4 v[186:189], v39, s[8:9] offset:384 nt
	global_load_dwordx4 v[190:193], v40, s[8:9] offset:384 nt
	global_load_dwordx4 v[194:197], v41, s[8:9] offset:384 nt
	s_waitcnt vmcnt(24)
	s_cmp_eq_u32 s25, 0
	s_movk_i32 s6, 0x0
	s_cmovk_i32 s6, 0x0
	s_add_u32 s6, s6, s24
	s_lshl_b32 s6, s6, s26
	s_add_u32 s14, s12, s6
	s_addc_u32 s15, s13, 0
	v_cvt_pk_bf16_f32 v46, v54, v58
	v_cvt_pk_bf16_f32 v47, v62, v66
	v_cvt_pk_bf16_f32 v48, v70, v74
	v_cvt_pk_bf16_f32 v49, v78, v82
	global_store_dwordx4 v42, v[46:49], s[14:15] nt
	v_cvt_pk_bf16_f32 v50, v55, v59
	v_cvt_pk_bf16_f32 v51, v63, v67
	v_cvt_pk_bf16_f32 v52, v71, v75
	v_cvt_pk_bf16_f32 v53, v79, v83
	global_store_dwordx4 v43, v[50:53], s[14:15] nt
	v_cvt_pk_bf16_f32 v46, v56, v60
	v_cvt_pk_bf16_f32 v47, v64, v68
	v_cvt_pk_bf16_f32 v48, v72, v76
	v_cvt_pk_bf16_f32 v49, v80, v84
	global_store_dwordx4 v44, v[46:49], s[14:15] nt
	v_cvt_pk_bf16_f32 v50, v57, v61
	v_cvt_pk_bf16_f32 v51, v65, v69
	v_cvt_pk_bf16_f32 v52, v73, v77
	v_cvt_pk_bf16_f32 v53, v81, v85
	global_store_dwordx4 v45, v[50:53], s[14:15] nt
	global_load_dwordx4 v[54:57], v34, s[8:9] offset:512 nt
	global_load_dwordx4 v[58:61], v35, s[8:9] offset:512 nt
	global_load_dwordx4 v[62:65], v36, s[8:9] offset:512 nt
	global_load_dwordx4 v[66:69], v37, s[8:9] offset:512 nt
	global_load_dwordx4 v[70:73], v38, s[8:9] offset:512 nt
	global_load_dwordx4 v[74:77], v39, s[8:9] offset:512 nt
	global_load_dwordx4 v[78:81], v40, s[8:9] offset:512 nt
	global_load_dwordx4 v[82:85], v41, s[8:9] offset:512 nt
	s_waitcnt vmcnt(28)
	s_cmp_eq_u32 s25, 0
	s_movk_i32 s6, 0x20
	s_cmovk_i32 s6, 0x20
	s_add_u32 s6, s6, s24
	s_lshl_b32 s6, s6, s26
	s_add_u32 s14, s12, s6
	s_addc_u32 s15, s13, 0
	v_cvt_pk_bf16_f32 v46, v86, v90
	v_cvt_pk_bf16_f32 v47, v94, v98
	v_cvt_pk_bf16_f32 v48, v102, v106
	v_cvt_pk_bf16_f32 v49, v110, v114
	global_store_dwordx4 v42, v[46:49], s[14:15] nt
	v_cvt_pk_bf16_f32 v50, v87, v91
	v_cvt_pk_bf16_f32 v51, v95, v99
	v_cvt_pk_bf16_f32 v52, v103, v107
	v_cvt_pk_bf16_f32 v53, v111, v115
	global_store_dwordx4 v43, v[50:53], s[14:15] nt
	v_cvt_pk_bf16_f32 v46, v88, v92
	v_cvt_pk_bf16_f32 v47, v96, v100
	v_cvt_pk_bf16_f32 v48, v104, v108
	v_cvt_pk_bf16_f32 v49, v112, v116
	global_store_dwordx4 v44, v[46:49], s[14:15] nt
	v_cvt_pk_bf16_f32 v50, v89, v93
	v_cvt_pk_bf16_f32 v51, v97, v101
	v_cvt_pk_bf16_f32 v52, v105, v109
	v_cvt_pk_bf16_f32 v53, v113, v117
	global_store_dwordx4 v45, v[50:53], s[14:15] nt
	global_load_dwordx4 v[86:89], v34, s[8:9] offset:640 nt
	global_load_dwordx4 v[90:93], v35, s[8:9] offset:640 nt
	global_load_dwordx4 v[94:97], v36, s[8:9] offset:640 nt
	global_load_dwordx4 v[98:101], v37, s[8:9] offset:640 nt
	global_load_dwordx4 v[102:105], v38, s[8:9] offset:640 nt
	global_load_dwordx4 v[106:109], v39, s[8:9] offset:640 nt
	global_load_dwordx4 v[110:113], v40, s[8:9] offset:640 nt
	global_load_dwordx4 v[114:117], v41, s[8:9] offset:640 nt
	s_waitcnt vmcnt(32)
	s_cmp_eq_u32 s25, 0
	s_movk_i32 s6, 0x40
	s_cmovk_i32 s6, 0x40
	s_add_u32 s6, s6, s24
	s_lshl_b32 s6, s6, s26
	s_add_u32 s14, s12, s6
	s_addc_u32 s15, s13, 0
	v_cvt_pk_bf16_f32 v46, v118, v122
	v_cvt_pk_bf16_f32 v47, v126, v130
	v_cvt_pk_bf16_f32 v48, v134, v138
	v_cvt_pk_bf16_f32 v49, v142, v146
	global_store_dwordx4 v42, v[46:49], s[14:15] nt
	v_cvt_pk_bf16_f32 v50, v119, v123
	v_cvt_pk_bf16_f32 v51, v127, v131
	v_cvt_pk_bf16_f32 v52, v135, v139
	v_cvt_pk_bf16_f32 v53, v143, v147
	global_store_dwordx4 v43, v[50:53], s[14:15] nt
	v_cvt_pk_bf16_f32 v46, v120, v124
	v_cvt_pk_bf16_f32 v47, v128, v132
	v_cvt_pk_bf16_f32 v48, v136, v140
	v_cvt_pk_bf16_f32 v49, v144, v148
	global_store_dwordx4 v44, v[46:49], s[14:15] nt
	v_cvt_pk_bf16_f32 v50, v121, v125
	v_cvt_pk_bf16_f32 v51, v129, v133
	v_cvt_pk_bf16_f32 v52, v137, v141
	v_cvt_pk_bf16_f32 v53, v145, v149
	global_store_dwordx4 v45, v[50:53], s[14:15] nt
	global_load_dwordx4 v[118:121], v34, s[8:9] offset:768 nt
	global_load_dwordx4 v[122:125], v35, s[8:9] offset:768 nt
	global_load_dwordx4 v[126:129], v36, s[8:9] offset:768 nt
	global_load_dwordx4 v[130:133], v37, s[8:9] offset:768 nt
	global_load_dwordx4 v[134:137], v38, s[8:9] offset:768 nt
	global_load_dwordx4 v[138:141], v39, s[8:9] offset:768 nt
	global_load_dwordx4 v[142:145], v40, s[8:9] offset:768 nt
	global_load_dwordx4 v[146:149], v41, s[8:9] offset:768 nt
	s_waitcnt vmcnt(36)
; #define GAS __attribute__((address_space(1)))
; #define LAS __attribute__((address_space(3)))
; #define LDS_WAIT() asm volatile("s_waitcnt lgkmcnt(0)" ::: "memory")
; __device__ __forceinline__ unsigned pk2(float lo, float hi) { unsigned r; asm("v_cvt_pk_bf16_f32 %0, %1, %2" : "=v"(r) : "v"(lo), "v"(hi)); return r; }
; __device__ __forceinline__ void t_load(const TItem& d, f32x4 (&r)[8], int lane) {
;     const float* p = d.W + (size_t)(d.k0 + (lane >> 3)) * d.N + d.n0 + (lane & 7) * 4;
; #pragma unroll
;     for (int i = 0; i < 8; ++i) r[i] = __builtin_nontemporal_load((const f32x4*)(p + (size_t)(8 * i) * d.N));
; }
; __device__ __forceinline__ void t_store(const TItem& d, const f32x4 (&r)[8], LAS float* scr, int lane) {
; #pragma unroll
;     for (int i = 0; i < 8; ++i) *(LAS f32x4*)(scr + (8 * i + (lane >> 3)) * 32 + (((lane & 7) * 4 + 8 * i) & 31)) = r[i];
;     LDS_WAIT(); asm volatile("" ::: "memory");
;     const int c = lane >> 3, nl = lane & 7;
; #pragma unroll
;     for (int j = 0; j < 4; ++j) { const int n = nl + 8 * j; const LAS float* s = scr + (8 * c) * 32 + ((n + 8 * c) & 31);
;         v4u o; o.x = pk2(s[0 * 32], s[1 * 32]); o.y = pk2(s[2 * 32], s[3 * 32]); o.z = pk2(s[4 * 32], s[5 * 32]); o.w = pk2(s[6 * 32], s[7 * 32]);
;         __builtin_nontemporal_store(o, (GAS v4u*)(d.WT + (size_t)t_drow(d.kind, d.n0 + n) * d.K + d.k0 + 8 * c)); }
;     LDS_WAIT(); asm volatile("" ::: "memory");
; }
; __global__ void __launch_bounds__(512, 2) mk_fwd(Params p_unused) {
;     ...
;             for (unsigned tb = grab(); tb < NTICK; tb = grab()) {
;                 TItem a0 = decode((int)(2u * tb)); TItem a1 = a0; a1.n0 += 32;
;                 f32x4 ra[8], rb[8], rc[8], rd[8]; t_load(a0, ra, lane); t_load(a1, rb, lane);
;                 _Pragma("unroll 1") for (unsigned u = 0; u < 8u; u += 2u) {
;                     const TItem b0 = decode((int)(2u * (tb + u + 1u))); TItem b1 = b0; b1.n0 += 32;
;                     t_load(b0, rc, lane); t_load(b1, rd, lane);
;                     t_store(a0, ra, scr, lane); t_store(a1, rb, scr, lane);
;                     if (u + 2u < 8u) { a0 = decode((int)(2u * (tb + u + 2u))); a1 = a0; a1.n0 += 32; t_load(a0, ra, lane); t_load(a1, rb, lane); }
;                     t_store(b0, rc, scr, lane); t_store(b1, rd, scr, lane);
;                 }
	s_cmp_eq_u32 s25, 0
	s_movk_i32 s6, 0x60
	s_cmovk_i32 s6, 0x60
	s_add_u32 s6, s6, s24
	s_lshl_b32 s6, s6, s26
	s_add_u32 s14, s12, s6
	s_addc_u32 s15, s13, 0
	v_cvt_pk_bf16_f32 v46, v166, v170
	v_cvt_pk_bf16_f32 v47, v174, v178
	v_cvt_pk_bf16_f32 v48, v182, v186
	v_cvt_pk_bf16_f32 v49, v190, v194
	global_store_dwordx4 v42, v[46:49], s[14:15] nt
	v_cvt_pk_bf16_f32 v50, v167, v171
	v_cvt_pk_bf16_f32 v51, v175, v179
	v_cvt_pk_bf16_f32 v52, v183, v187
	v_cvt_pk_bf16_f32 v53, v191, v195
	global_store_dwordx4 v43, v[50:53], s[14:15] nt
	v_cvt_pk_bf16_f32 v46, v168, v172
	v_cvt_pk_bf16_f32 v47, v176, v180
	v_cvt_pk_bf16_f32 v48, v184, v188
	v_cvt_pk_bf16_f32 v49, v192, v196
	global_store_dwordx4 v44, v[46:49], s[14:15] nt
	v_cvt_pk_bf16_f32 v50, v169, v173
	v_cvt_pk_bf16_f32 v51, v177, v181
	v_cvt_pk_bf16_f32 v52, v185, v189
	v_cvt_pk_bf16_f32 v53, v193, v197
	global_store_dwordx4 v45, v[50:53], s[14:15] nt
	global_load_dwordx4 v[166:169], v34, s[8:9] offset:896 nt
	global_load_dwordx4 v[170:173], v35, s[8:9] offset:896 nt
	global_load_dwordx4 v[174:177], v36, s[8:9] offset:896 nt
	global_load_dwordx4 v[178:181], v37, s[8:9] offset:896 nt
	global_load_dwordx4 v[182:185], v38, s[8:9] offset:896 nt
	global_load_dwordx4 v[186:189], v39, s[8:9] offset:896 nt
	global_load_dwordx4 v[190:193], v40, s[8:9] offset:896 nt
	global_load_dwordx4 v[194:197], v41, s[8:9] offset:896 nt
	s_waitcnt vmcnt(36)
	s_cmp_eq_u32 s25, 0
	s_movk_i32 s6, 0x80
	s_cmovk_i32 s6, 0x100
	s_add_u32 s6, s6, s24
	s_lshl_b32 s6, s6, s26
	s_add_u32 s14, s12, s6
	s_addc_u32 s15, s13, 0
	v_cvt_pk_bf16_f32 v46, v54, v58
	v_cvt_pk_bf16_f32 v47, v62, v66
	v_cvt_pk_bf16_f32 v48, v70, v74
	v_cvt_pk_bf16_f32 v49, v78, v82
	global_store_dwordx4 v42, v[46:49], s[14:15] nt
	v_cvt_pk_bf16_f32 v50, v55, v59
	v_cvt_pk_bf16_f32 v51, v63, v67
	v_cvt_pk_bf16_f32 v52, v71, v75
	v_cvt_pk_bf16_f32 v53, v79, v83
	global_store_dwordx4 v43, v[50:53], s[14:15] nt
	v_cvt_pk_bf16_f32 v46, v56, v60
	v_cvt_pk_bf16_f32 v47, v64, v68
	v_cvt_pk_bf16_f32 v48, v72, v76
	v_cvt_pk_bf16_f32 v49, v80, v84
	global_store_dwordx4 v44, v[46:49], s[14:15] nt
	v_cvt_pk_bf16_f32 v50, v57, v61
	v_cvt_pk_bf16_f32 v51, v65, v69
	v_cvt_pk_bf16_f32 v52, v73, v77
	v_cvt_pk_bf16_f32 v53, v81, v85
	global_store_dwordx4 v45, v[50:53], s[14:15] nt
	global_load_dwordx4 v[54:57], v34, s[8:9] offset:1024 nt
	global_load_dwordx4 v[58:61], v35, s[8:9] offset:1024 nt
	global_load_dwordx4 v[62:65], v36, s[8:9] offset:1024 nt
	global_load_dwordx4 v[66:69], v37, s[8:9] offset:1024 nt
	global_load_dwordx4 v[70:73], v38, s[8:9] offset:1024 nt
	global_load_dwordx4 v[74:77], v39, s[8:9] offset:1024 nt
	global_load_dwordx4 v[78:81], v40, s[8:9] offset:1024 nt
	global_load_dwordx4 v[82:85], v41, s[8:9] offset:1024 nt
	s_waitcnt vmcnt(36)
	s_cmp_eq_u32 s25, 0
	s_movk_i32 s6, 0xa0
	s_cmovk_i32 s6, 0x120
	s_add_u32 s6, s6, s24
	s_lshl_b32 s6, s6, s26
	s_add_u32 s14, s12, s6
	s_addc_u32 s15, s13, 0
	v_cvt_pk_bf16_f32 v46, v86, v90
	v_cvt_pk_bf16_f32 v47, v94, v98
	v_cvt_pk_bf16_f32 v48, v102, v106
	v_cvt_pk_bf16_f32 v49, v110, v114
	global_store_dwordx4 v42, v[46:49], s[14:15] nt
	v_cvt_pk_bf16_f32 v50, v87, v91
	v_cvt_pk_bf16_f32 v51, v95, v99
	v_cvt_pk_bf16_f32 v52, v103, v107
	v_cvt_pk_bf16_f32 v53, v111, v115
	global_store_dwordx4 v43, v[50:53], s[14:15] nt
	v_cvt_pk_bf16_f32 v46, v88, v92
	v_cvt_pk_bf16_f32 v47, v96, v100
	v_cvt_pk_bf16_f32 v48, v104, v108
	v_cvt_pk_bf16_f32 v49, v112, v116
	global_store_dwordx4 v44, v[46:49], s[14:15] nt
	v_cvt_pk_bf16_f32 v50, v89, v93
	v_cvt_pk_bf16_f32 v51, v97, v101
	v_cvt_pk_bf16_f32 v52, v105, v109
	v_cvt_pk_bf16_f32 v53, v113, v117
	global_store_dwordx4 v45, v[50:53], s[14:15] nt
	global_load_dwordx4 v[86:89], v34, s[8:9] offset:1152 nt
	global_load_dwordx4 v[90:93], v35, s[8:9] offset:1152 nt
	global_load_dwordx4 v[94:97], v36, s[8:9] offset:1152 nt
	global_load_dwordx4 v[98:101], v37, s[8:9] offset:1152 nt
	global_load_dwordx4 v[102:105], v38, s[8:9] offset:1152 nt
	global_load_dwordx4 v[106:109], v39, s[8:9] offset:1152 nt
	global_load_dwordx4 v[110:113], v40, s[8:9] offset:1152 nt
	global_load_dwordx4 v[114:117], v41, s[8:9] offset:1152 nt
	s_waitcnt vmcnt(36)
	s_cmp_eq_u32 s25, 0
	s_movk_i32 s6, 0xc0
	s_cmovk_i32 s6, 0x140
	s_add_u32 s6, s6, s24
	s_lshl_b32 s6, s6, s26
	s_add_u32 s14, s12, s6
	s_addc_u32 s15, s13, 0
	v_cvt_pk_bf16_f32 v46, v118, v122
	v_cvt_pk_bf16_f32 v47, v126, v130
	v_cvt_pk_bf16_f32 v48, v134, v138
	v_cvt_pk_bf16_f32 v49, v142, v146
	global_store_dwordx4 v42, v[46:49], s[14:15] nt
	v_cvt_pk_bf16_f32 v50, v119, v123
	v_cvt_pk_bf16_f32 v51, v127, v131
	v_cvt_pk_bf16_f32 v52, v135, v139
	v_cvt_pk_bf16_f32 v53, v143, v147
	global_store_dwordx4 v43, v[50:53], s[14:15] nt
	v_cvt_pk_bf16_f32 v46, v120, v124
	v_cvt_pk_bf16_f32 v47, v128, v132
	v_cvt_pk_bf16_f32 v48, v136, v140
	v_cvt_pk_bf16_f32 v49, v144, v148
	global_store_dwordx4 v44, v[46:49], s[14:15] nt
	v_cvt_pk_bf16_f32 v50, v121, v125
	v_cvt_pk_bf16_f32 v51, v129, v133
	v_cvt_pk_bf16_f32 v52, v137, v141
	v_cvt_pk_bf16_f32 v53, v145, v149
	global_store_dwordx4 v45, v[50:53], s[14:15] nt
	global_load_dwordx4 v[118:121], v34, s[8:9] offset:1280 nt
	global_load_dwordx4 v[122:125], v35, s[8:9] offset:1280 nt
	global_load_dwordx4 v[126:129], v36, s[8:9] offset:1280 nt
	global_load_dwordx4 v[130:133], v37, s[8:9] offset:1280 nt
	global_load_dwordx4 v[134:137], v38, s[8:9] offset:1280 nt
	global_load_dwordx4 v[138:141], v39, s[8:9] offset:1280 nt
	global_load_dwordx4 v[142:145], v40, s[8:9] offset:1280 nt
	global_load_dwordx4 v[146:149], v41, s[8:9] offset:1280 nt
	s_waitcnt vmcnt(36)
; #define GAS __attribute__((address_space(1)))
; #define LAS __attribute__((address_space(3)))
; #define LDS_WAIT() asm volatile("s_waitcnt lgkmcnt(0)" ::: "memory")
; __device__ __forceinline__ unsigned pk2(float lo, float hi) { unsigned r; asm("v_cvt_pk_bf16_f32 %0, %1, %2" : "=v"(r) : "v"(lo), "v"(hi)); return r; }
; __device__ __forceinline__ void t_load(const TItem& d, f32x4 (&r)[8], int lane) {
;     const float* p = d.W + (size_t)(d.k0 + (lane >> 3)) * d.N + d.n0 + (lane & 7) * 4;
; #pragma unroll
;     for (int i = 0; i < 8; ++i) r[i] = __builtin_nontemporal_load((const f32x4*)(p + (size_t)(8 * i) * d.N));
; }
; __device__ __forceinline__ void t_store(const TItem& d, const f32x4 (&r)[8], LAS float* scr, int lane) {
; #pragma unroll
;     for (int i = 0; i < 8; ++i) *(LAS f32x4*)(scr + (8 * i + (lane >> 3)) * 32 + (((lane & 7) * 4 + 8 * i) & 31)) = r[i];
;     LDS_WAIT(); asm volatile("" ::: "memory");
;     const int c = lane >> 3, nl = lane & 7;
; #pragma unroll
;     for (int j = 0; j < 4; ++j) { const int n = nl + 8 * j; const LAS float* s = scr + (8 * c) * 32 + ((n + 8 * c) & 31);
;         v4u o; o.x = pk2(s[0 * 32], s[1 * 32]); o.y = pk2(s[2 * 32], s[3 * 32]); o.z = pk2(s[4 * 32], s[5 * 32]); o.w = pk2(s[6 * 32], s[7 * 32]);
;         __builtin_nontemporal_store(o, (GAS v4u*)(d.WT + (size_t)t_drow(d.kind, d.n0 + n) * d.K + d.k0 + 8 * c)); }
;     LDS_WAIT(); asm volatile("" ::: "memory");
; }
; __global__ void __launch_bounds__(512, 2) mk_fwd(Params p_unused) {
;     ...
;             for (unsigned tb = grab(); tb < NTICK; tb = grab()) {
;                 TItem a0 = decode((int)(2u * tb)); TItem a1 = a0; a1.n0 += 32;
;                 f32x4 ra[8], rb[8], rc[8], rd[8]; t_load(a0, ra, lane); t_load(a1, rb, lane);
;                 _Pragma("unroll 1") for (unsigned u = 0; u < 8u; u += 2u) {
;                     const TItem b0 = decode((int)(2u * (tb + u + 1u))); TItem b1 = b0; b1.n0 += 32;
;                     t_load(b0, rc, lane); t_load(b1, rd, lane);
;                     t_store(a0, ra, scr, lane); t_store(a1, rb, scr, lane);
;                     if (u + 2u < 8u) { a0 = decode((int)(2u * (tb + u + 2u))); a1 = a0; a1.n0 += 32; t_load(a0, ra, lane); t_load(a1, rb, lane); }
;                     t_store(b0, rc, scr, lane); t_store(b1, rd, scr, lane);
;                 }
	s_cmp_eq_u32 s25, 0
	s_movk_i32 s6, 0xe0
	s_cmovk_i32 s6, 0x160
	s_add_u32 s6, s6, s24
	s_lshl_b32 s6, s6, s26
	s_add_u32 s14, s12, s6
	s_addc_u32 s15, s13, 0
	v_cvt_pk_bf16_f32 v46, v166, v170
	v_cvt_pk_bf16_f32 v47, v174, v178
	v_cvt_pk_bf16_f32 v48, v182, v186
	v_cvt_pk_bf16_f32 v49, v190, v194
	global_store_dwordx4 v42, v[46:49], s[14:15] nt
	v_cvt_pk_bf16_f32 v50, v167, v171
	v_cvt_pk_bf16_f32 v51, v175, v179
	v_cvt_pk_bf16_f32 v52, v183, v187
	v_cvt_pk_bf16_f32 v53, v191, v195
	global_store_dwordx4 v43, v[50:53], s[14:15] nt
	v_cvt_pk_bf16_f32 v46, v168, v172
	v_cvt_pk_bf16_f32 v47, v176, v180
	v_cvt_pk_bf16_f32 v48, v184, v188
	v_cvt_pk_bf16_f32 v49, v192, v196
	global_store_dwordx4 v44, v[46:49], s[14:15] nt
	v_cvt_pk_bf16_f32 v50, v169, v173
	v_cvt_pk_bf16_f32 v51, v177, v181
	v_cvt_pk_bf16_f32 v52, v185, v189
	v_cvt_pk_bf16_f32 v53, v193, v197
	global_store_dwordx4 v45, v[50:53], s[14:15] nt
	global_load_dwordx4 v[166:169], v34, s[8:9] offset:1408 nt
	global_load_dwordx4 v[170:173], v35, s[8:9] offset:1408 nt
	global_load_dwordx4 v[174:177], v36, s[8:9] offset:1408 nt
	global_load_dwordx4 v[178:181], v37, s[8:9] offset:1408 nt
	global_load_dwordx4 v[182:185], v38, s[8:9] offset:1408 nt
	global_load_dwordx4 v[186:189], v39, s[8:9] offset:1408 nt
	global_load_dwordx4 v[190:193], v40, s[8:9] offset:1408 nt
	global_load_dwordx4 v[194:197], v41, s[8:9] offset:1408 nt
	s_waitcnt vmcnt(36)
	s_cmp_eq_u32 s25, 0
	s_movk_i32 s6, 0x100
	s_cmovk_i32 s6, 0x200
	s_add_u32 s6, s6, s24
	s_lshl_b32 s6, s6, s26
	s_add_u32 s14, s12, s6
	s_addc_u32 s15, s13, 0
	v_cvt_pk_bf16_f32 v46, v54, v58
	v_cvt_pk_bf16_f32 v47, v62, v66
	v_cvt_pk_bf16_f32 v48, v70, v74
	v_cvt_pk_bf16_f32 v49, v78, v82
	global_store_dwordx4 v42, v[46:49], s[14:15] nt
	v_cvt_pk_bf16_f32 v50, v55, v59
	v_cvt_pk_bf16_f32 v51, v63, v67
	v_cvt_pk_bf16_f32 v52, v71, v75
	v_cvt_pk_bf16_f32 v53, v79, v83
	global_store_dwordx4 v43, v[50:53], s[14:15] nt
	v_cvt_pk_bf16_f32 v46, v56, v60
	v_cvt_pk_bf16_f32 v47, v64, v68
	v_cvt_pk_bf16_f32 v48, v72, v76
	v_cvt_pk_bf16_f32 v49, v80, v84
	global_store_dwordx4 v44, v[46:49], s[14:15] nt
	v_cvt_pk_bf16_f32 v50, v57, v61
	v_cvt_pk_bf16_f32 v51, v65, v69
	v_cvt_pk_bf16_f32 v52, v73, v77
	v_cvt_pk_bf16_f32 v53, v81, v85
	global_store_dwordx4 v45, v[50:53], s[14:15] nt
	global_load_dwordx4 v[54:57], v34, s[8:9] offset:1536 nt
	global_load_dwordx4 v[58:61], v35, s[8:9] offset:1536 nt
	global_load_dwordx4 v[62:65], v36, s[8:9] offset:1536 nt
	global_load_dwordx4 v[66:69], v37, s[8:9] offset:1536 nt
	global_load_dwordx4 v[70:73], v38, s[8:9] offset:1536 nt
	global_load_dwordx4 v[74:77], v39, s[8:9] offset:1536 nt
	global_load_dwordx4 v[78:81], v40, s[8:9] offset:1536 nt
	global_load_dwordx4 v[82:85], v41, s[8:9] offset:1536 nt
	s_waitcnt vmcnt(36)
	s_cmp_eq_u32 s25, 0
	s_movk_i32 s6, 0x120
	s_cmovk_i32 s6, 0x220
	s_add_u32 s6, s6, s24
	s_lshl_b32 s6, s6, s26
	s_add_u32 s14, s12, s6
	s_addc_u32 s15, s13, 0
	v_cvt_pk_bf16_f32 v46, v86, v90
	v_cvt_pk_bf16_f32 v47, v94, v98
	v_cvt_pk_bf16_f32 v48, v102, v106
	v_cvt_pk_bf16_f32 v49, v110, v114
	global_store_dwordx4 v42, v[46:49], s[14:15] nt
	v_cvt_pk_bf16_f32 v50, v87, v91
	v_cvt_pk_bf16_f32 v51, v95, v99
	v_cvt_pk_bf16_f32 v52, v103, v107
	v_cvt_pk_bf16_f32 v53, v111, v115
	global_store_dwordx4 v43, v[50:53], s[14:15] nt
	v_cvt_pk_bf16_f32 v46, v88, v92
	v_cvt_pk_bf16_f32 v47, v96, v100
	v_cvt_pk_bf16_f32 v48, v104, v108
	v_cvt_pk_bf16_f32 v49, v112, v116
	global_store_dwordx4 v44, v[46:49], s[14:15] nt
	v_cvt_pk_bf16_f32 v50, v89, v93
	v_cvt_pk_bf16_f32 v51, v97, v101
	v_cvt_pk_bf16_f32 v52, v105, v109
	v_cvt_pk_bf16_f32 v53, v113, v117
	global_store_dwordx4 v45, v[50:53], s[14:15] nt
	global_load_dwordx4 v[86:89], v34, s[8:9] offset:1664 nt
	global_load_dwordx4 v[90:93], v35, s[8:9] offset:1664 nt
	global_load_dwordx4 v[94:97], v36, s[8:9] offset:1664 nt
	global_load_dwordx4 v[98:101], v37, s[8:9] offset:1664 nt
	global_load_dwordx4 v[102:105], v38, s[8:9] offset:1664 nt
	global_load_dwordx4 v[106:109], v39, s[8:9] offset:1664 nt
	global_load_dwordx4 v[110:113], v40, s[8:9] offset:1664 nt
	global_load_dwordx4 v[114:117], v41, s[8:9] offset:1664 nt
	s_waitcnt vmcnt(36)
	s_cmp_eq_u32 s25, 0
	s_movk_i32 s6, 0x140
	s_cmovk_i32 s6, 0x240
	s_add_u32 s6, s6, s24
	s_lshl_b32 s6, s6, s26
	s_add_u32 s14, s12, s6
	s_addc_u32 s15, s13, 0
	v_cvt_pk_bf16_f32 v46, v118, v122
	v_cvt_pk_bf16_f32 v47, v126, v130
	v_cvt_pk_bf16_f32 v48, v134, v138
	v_cvt_pk_bf16_f32 v49, v142, v146
	global_store_dwordx4 v42, v[46:49], s[14:15] nt
	v_cvt_pk_bf16_f32 v50, v119, v123
	v_cvt_pk_bf16_f32 v51, v127, v131
	v_cvt_pk_bf16_f32 v52, v135, v139
	v_cvt_pk_bf16_f32 v53, v143, v147
	global_store_dwordx4 v43, v[50:53], s[14:15] nt
	v_cvt_pk_bf16_f32 v46, v120, v124
	v_cvt_pk_bf16_f32 v47, v128, v132
	v_cvt_pk_bf16_f32 v48, v136, v140
	v_cvt_pk_bf16_f32 v49, v144, v148
	global_store_dwordx4 v44, v[46:49], s[14:15] nt
	v_cvt_pk_bf16_f32 v50, v121, v125
	v_cvt_pk_bf16_f32 v51, v129, v133
	v_cvt_pk_bf16_f32 v52, v137, v141
	v_cvt_pk_bf16_f32 v53, v145, v149
	global_store_dwordx4 v45, v[50:53], s[14:15] nt
	global_load_dwordx4 v[118:121], v34, s[8:9] offset:1792 nt
	global_load_dwordx4 v[122:125], v35, s[8:9] offset:1792 nt
	global_load_dwordx4 v[126:129], v36, s[8:9] offset:1792 nt
	global_load_dwordx4 v[130:133], v37, s[8:9] offset:1792 nt
	global_load_dwordx4 v[134:137], v38, s[8:9] offset:1792 nt
	global_load_dwordx4 v[138:141], v39, s[8:9] offset:1792 nt
	global_load_dwordx4 v[142:145], v40, s[8:9] offset:1792 nt
	global_load_dwordx4 v[146:149], v41, s[8:9] offset:1792 nt
	s_waitcnt vmcnt(36)
; #define GAS __attribute__((address_space(1)))
; #define LAS __attribute__((address_space(3)))
; #define LDS_WAIT() asm volatile("s_waitcnt lgkmcnt(0)" ::: "memory")
; __device__ __forceinline__ unsigned pk2(float lo, float hi) { unsigned r; asm("v_cvt_pk_bf16_f32 %0, %1, %2" : "=v"(r) : "v"(lo), "v"(hi)); return r; }
; __device__ __forceinline__ void t_load(const TItem& d, f32x4 (&r)[8], int lane) {
;     const float* p = d.W + (size_t)(d.k0 + (lane >> 3)) * d.N + d.n0 + (lane & 7) * 4;
; #pragma unroll
;     for (int i = 0; i < 8; ++i) r[i] = __builtin_nontemporal_load((const f32x4*)(p + (size_t)(8 * i) * d.N));
; }
; __device__ __forceinline__ void t_store(const TItem& d, const f32x4 (&r)[8], LAS float* scr, int lane) {
; #pragma unroll
;     for (int i = 0; i < 8; ++i) *(LAS f32x4*)(scr + (8 * i + (lane >> 3)) * 32 + (((lane & 7) * 4 + 8 * i) & 31)) = r[i];
;     LDS_WAIT(); asm volatile("" ::: "memory");
;     const int c = lane >> 3, nl = lane & 7;
; #pragma unroll
;     for (int j = 0; j < 4; ++j) { const int n = nl + 8 * j; const LAS float* s = scr + (8 * c) * 32 + ((n + 8 * c) & 31);
;         v4u o; o.x = pk2(s[0 * 32], s[1 * 32]); o.y = pk2(s[2 * 32], s[3 * 32]); o.z = pk2(s[4 * 32], s[5 * 32]); o.w = pk2(s[6 * 32], s[7 * 32]);
;         __builtin_nontemporal_store(o, (GAS v4u*)(d.WT + (size_t)t_drow(d.kind, d.n0 + n) * d.K + d.k0 + 8 * c)); }
;     LDS_WAIT(); asm volatile("" ::: "memory");
; }
; __global__ void __launch_bounds__(512, 2) mk_fwd(Params p_unused) {
;     ...
;             for (unsigned tb = grab(); tb < NTICK; tb = grab()) {
;                 TItem a0 = decode((int)(2u * tb)); TItem a1 = a0; a1.n0 += 32;
;                 f32x4 ra[8], rb[8], rc[8], rd[8]; t_load(a0, ra, lane); t_load(a1, rb, lane);
;                 _Pragma("unroll 1") for (unsigned u = 0; u < 8u; u += 2u) {
;                     const TItem b0 = decode((int)(2u * (tb + u + 1u))); TItem b1 = b0; b1.n0 += 32;
;                     t_load(b0, rc, lane); t_load(b1, rd, lane);
;                     t_store(a0, ra, scr, lane); t_store(a1, rb, scr, lane);
;                     if (u + 2u < 8u) { a0 = decode((int)(2u * (tb + u + 2u))); a1 = a0; a1.n0 += 32; t_load(a0, ra, lane); t_load(a1, rb, lane); }
;                     t_store(b0, rc, scr, lane); t_store(b1, rd, scr, lane);
;                 }
	s_cmp_eq_u32 s25, 0
	s_movk_i32 s6, 0x160
	s_cmovk_i32 s6, 0x260
	s_add_u32 s6, s6, s24
	s_lshl_b32 s6, s6, s26
	s_add_u32 s14, s12, s6
	s_addc_u32 s15, s13, 0
	v_cvt_pk_bf16_f32 v46, v166, v170
	v_cvt_pk_bf16_f32 v47, v174, v178
	v_cvt_pk_bf16_f32 v48, v182, v186
	v_cvt_pk_bf16_f32 v49, v190, v194
	global_store_dwordx4 v42, v[46:49], s[14:15] nt
	v_cvt_pk_bf16_f32 v50, v167, v171
	v_cvt_pk_bf16_f32 v51, v175, v179
	v_cvt_pk_bf16_f32 v52, v183, v187
	v_cvt_pk_bf16_f32 v53, v191, v195
	global_store_dwordx4 v43, v[50:53], s[14:15] nt
	v_cvt_pk_bf16_f32 v46, v168, v172
	v_cvt_pk_bf16_f32 v47, v176, v180
	v_cvt_pk_bf16_f32 v48, v184, v188
	v_cvt_pk_bf16_f32 v49, v192, v196
	global_store_dwordx4 v44, v[46:49], s[14:15] nt
	v_cvt_pk_bf16_f32 v50, v169, v173
	v_cvt_pk_bf16_f32 v51, v177, v181
	v_cvt_pk_bf16_f32 v52, v185, v189
	v_cvt_pk_bf16_f32 v53, v193, v197
	global_store_dwordx4 v45, v[50:53], s[14:15] nt
	global_load_dwordx4 v[166:169], v34, s[8:9] offset:1920 nt
	global_load_dwordx4 v[170:173], v35, s[8:9] offset:1920 nt
	global_load_dwordx4 v[174:177], v36, s[8:9] offset:1920 nt
	global_load_dwordx4 v[178:181], v37, s[8:9] offset:1920 nt
	global_load_dwordx4 v[182:185], v38, s[8:9] offset:1920 nt
	global_load_dwordx4 v[186:189], v39, s[8:9] offset:1920 nt
	global_load_dwordx4 v[190:193], v40, s[8:9] offset:1920 nt
	global_load_dwordx4 v[194:197], v41, s[8:9] offset:1920 nt
	s_waitcnt vmcnt(36)
	s_cmp_eq_u32 s25, 0
	s_movk_i32 s6, 0x180
	s_cmovk_i32 s6, 0x300
	s_add_u32 s6, s6, s24
	s_lshl_b32 s6, s6, s26
	s_add_u32 s14, s12, s6
	s_addc_u32 s15, s13, 0
	v_cvt_pk_bf16_f32 v46, v54, v58
	v_cvt_pk_bf16_f32 v47, v62, v66
	v_cvt_pk_bf16_f32 v48, v70, v74
	v_cvt_pk_bf16_f32 v49, v78, v82
	global_store_dwordx4 v42, v[46:49], s[14:15] nt
	v_cvt_pk_bf16_f32 v50, v55, v59
	v_cvt_pk_bf16_f32 v51, v63, v67
	v_cvt_pk_bf16_f32 v52, v71, v75
	v_cvt_pk_bf16_f32 v53, v79, v83
	global_store_dwordx4 v43, v[50:53], s[14:15] nt
	v_cvt_pk_bf16_f32 v46, v56, v60
	v_cvt_pk_bf16_f32 v47, v64, v68
	v_cvt_pk_bf16_f32 v48, v72, v76
	v_cvt_pk_bf16_f32 v49, v80, v84
	global_store_dwordx4 v44, v[46:49], s[14:15] nt
	v_cvt_pk_bf16_f32 v50, v57, v61
	v_cvt_pk_bf16_f32 v51, v65, v69
	v_cvt_pk_bf16_f32 v52, v73, v77
	v_cvt_pk_bf16_f32 v53, v81, v85
	global_store_dwordx4 v45, v[50:53], s[14:15] nt
	global_load_dwordx4 v[54:57], v34, s[8:9] offset:2048 nt
	global_load_dwordx4 v[58:61], v35, s[8:9] offset:2048 nt
	global_load_dwordx4 v[62:65], v36, s[8:9] offset:2048 nt
	global_load_dwordx4 v[66:69], v37, s[8:9] offset:2048 nt
	global_load_dwordx4 v[70:73], v38, s[8:9] offset:2048 nt
	global_load_dwordx4 v[74:77], v39, s[8:9] offset:2048 nt
	global_load_dwordx4 v[78:81], v40, s[8:9] offset:2048 nt
	global_load_dwordx4 v[82:85], v41, s[8:9] offset:2048 nt
	s_waitcnt vmcnt(36)
	s_cmp_eq_u32 s25, 0
	s_movk_i32 s6, 0x1a0
	s_cmovk_i32 s6, 0x320
	s_add_u32 s6, s6, s24
	s_lshl_b32 s6, s6, s26
	s_add_u32 s14, s12, s6
	s_addc_u32 s15, s13, 0
	v_cvt_pk_bf16_f32 v46, v86, v90
	v_cvt_pk_bf16_f32 v47, v94, v98
	v_cvt_pk_bf16_f32 v48, v102, v106
	v_cvt_pk_bf16_f32 v49, v110, v114
	global_store_dwordx4 v42, v[46:49], s[14:15] nt
	v_cvt_pk_bf16_f32 v50, v87, v91
	v_cvt_pk_bf16_f32 v51, v95, v99
	v_cvt_pk_bf16_f32 v52, v103, v107
	v_cvt_pk_bf16_f32 v53, v111, v115
	global_store_dwordx4 v43, v[50:53], s[14:15] nt
	v_cvt_pk_bf16_f32 v46, v88, v92
	v_cvt_pk_bf16_f32 v47, v96, v100
	v_cvt_pk_bf16_f32 v48, v104, v108
	v_cvt_pk_bf16_f32 v49, v112, v116
	global_store_dwordx4 v44, v[46:49], s[14:15] nt
	v_cvt_pk_bf16_f32 v50, v89, v93
	v_cvt_pk_bf16_f32 v51, v97, v101
	v_cvt_pk_bf16_f32 v52, v105, v109
	v_cvt_pk_bf16_f32 v53, v113, v117
	global_store_dwordx4 v45, v[50:53], s[14:15] nt
	global_load_dwordx4 v[86:89], v34, s[8:9] offset:2176 nt
	global_load_dwordx4 v[90:93], v35, s[8:9] offset:2176 nt
	global_load_dwordx4 v[94:97], v36, s[8:9] offset:2176 nt
	global_load_dwordx4 v[98:101], v37, s[8:9] offset:2176 nt
	global_load_dwordx4 v[102:105], v38, s[8:9] offset:2176 nt
	global_load_dwordx4 v[106:109], v39, s[8:9] offset:2176 nt
	global_load_dwordx4 v[110:113], v40, s[8:9] offset:2176 nt
	global_load_dwordx4 v[114:117], v41, s[8:9] offset:2176 nt
	s_waitcnt vmcnt(36)
	s_cmp_eq_u32 s25, 0
	s_movk_i32 s6, 0x1c0
	s_cmovk_i32 s6, 0x340
	s_add_u32 s6, s6, s24
	s_lshl_b32 s6, s6, s26
	s_add_u32 s14, s12, s6
	s_addc_u32 s15, s13, 0
	v_cvt_pk_bf16_f32 v46, v118, v122
	v_cvt_pk_bf16_f32 v47, v126, v130
	v_cvt_pk_bf16_f32 v48, v134, v138
	v_cvt_pk_bf16_f32 v49, v142, v146
	global_store_dwordx4 v42, v[46:49], s[14:15] nt
	v_cvt_pk_bf16_f32 v50, v119, v123
	v_cvt_pk_bf16_f32 v51, v127, v131
	v_cvt_pk_bf16_f32 v52, v135, v139
	v_cvt_pk_bf16_f32 v53, v143, v147
	global_store_dwordx4 v43, v[50:53], s[14:15] nt
	v_cvt_pk_bf16_f32 v46, v120, v124
	v_cvt_pk_bf16_f32 v47, v128, v132
	v_cvt_pk_bf16_f32 v48, v136, v140
	v_cvt_pk_bf16_f32 v49, v144, v148
	global_store_dwordx4 v44, v[46:49], s[14:15] nt
	v_cvt_pk_bf16_f32 v50, v121, v125
	v_cvt_pk_bf16_f32 v51, v129, v133
	v_cvt_pk_bf16_f32 v52, v137, v141
	v_cvt_pk_bf16_f32 v53, v145, v149
	global_store_dwordx4 v45, v[50:53], s[14:15] nt
	global_load_dwordx4 v[118:121], v34, s[8:9] offset:2304 nt
	global_load_dwordx4 v[122:125], v35, s[8:9] offset:2304 nt
	global_load_dwordx4 v[126:129], v36, s[8:9] offset:2304 nt
	global_load_dwordx4 v[130:133], v37, s[8:9] offset:2304 nt
	global_load_dwordx4 v[134:137], v38, s[8:9] offset:2304 nt
	global_load_dwordx4 v[138:141], v39, s[8:9] offset:2304 nt
	global_load_dwordx4 v[142:145], v40, s[8:9] offset:2304 nt
	global_load_dwordx4 v[146:149], v41, s[8:9] offset:2304 nt
	s_waitcnt vmcnt(36)
; #define GAS __attribute__((address_space(1)))
; #define LAS __attribute__((address_space(3)))
; #define LDS_WAIT() asm volatile("s_waitcnt lgkmcnt(0)" ::: "memory")
; __device__ __forceinline__ unsigned pk2(float lo, float hi) { unsigned r; asm("v_cvt_pk_bf16_f32 %0, %1, %2" : "=v"(r) : "v"(lo), "v"(hi)); return r; }
; __device__ __forceinline__ void t_load(const TItem& d, f32x4 (&r)[8], int lane) {
;     const float* p = d.W + (size_t)(d.k0 + (lane >> 3)) * d.N + d.n0 + (lane & 7) * 4;
; #pragma unroll
;     for (int i = 0; i < 8; ++i) r[i] = __builtin_nontemporal_load((const f32x4*)(p + (size_t)(8 * i) * d.N));
; }
; __device__ __forceinline__ void t_store(const TItem& d, const f32x4 (&r)[8], LAS float* scr, int lane) {
; #pragma unroll
;     for (int i = 0; i < 8; ++i) *(LAS f32x4*)(scr + (8 * i + (lane >> 3)) * 32 + (((lane & 7) * 4 + 8 * i) & 31)) = r[i];
;     LDS_WAIT(); asm volatile("" ::: "memory");
;     const int c = lane >> 3, nl = lane & 7;
; #pragma unroll
;     for (int j = 0; j < 4; ++j) { const int n = nl + 8 * j; const LAS float* s = scr + (8 * c) * 32 + ((n + 8 * c) & 31);
;         v4u o; o.x = pk2(s[0 * 32], s[1 * 32]); o.y = pk2(s[2 * 32], s[3 * 32]); o.z = pk2(s[4 * 32], s[5 * 32]); o.w = pk2(s[6 * 32], s[7 * 32]);
;         __builtin_nontemporal_store(o, (GAS v4u*)(d.WT + (size_t)t_drow(d.kind, d.n0 + n) * d.K + d.k0 + 8 * c)); }
; __global__ void __launch_bounds__(512, 2) mk_fwd(Params p_unused) {
;     ...
;             for (unsigned tb = grab(); tb < NTICK; tb = grab()) {
;                 TItem a0 = decode((int)(2u * tb)); TItem a1 = a0; a1.n0 += 32;
;                 f32x4 ra[8], rb[8], rc[8], rd[8]; t_load(a0, ra, lane); t_load(a1, rb, lane);
;                 _Pragma("unroll 1") for (unsigned u = 0; u < 8u; u += 2u) {
;                     const TItem b0 = decode((int)(2u * (tb + u + 1u))); TItem b1 = b0; b1.n0 += 32;
;                     t_load(b0, rc, lane); t_load(b1, rd, lane);
;                     t_store(a0, ra, scr, lane); t_store(a1, rb, scr, lane);
;                     if (u + 2u < 8u) { a0 = decode((int)(2u * (tb + u + 2u))); a1 = a0; a1.n0 += 32; t_load(a0, ra, lane); t_load(a1, rb, lane); }
;                     t_store(b0, rc, scr, lane); t_store(b1, rd, scr, lane);
;                 }
	s_cmp_eq_u32 s25, 0
	s_movk_i32 s6, 0x1e0
	s_cmovk_i32 s6, 0x360
	s_add_u32 s6, s6, s24
	s_lshl_b32 s6, s6, s26
	s_add_u32 s14, s12, s6
	s_addc_u32 s15, s13, 0
	v_cvt_pk_bf16_f32 v46, v166, v170
	v_cvt_pk_bf16_f32 v47, v174, v178
	v_cvt_pk_bf16_f32 v48, v182, v186
	v_cvt_pk_bf16_f32 v49, v190, v194
	global_store_dwordx4 v42, v[46:49], s[14:15] nt
	v_cvt_pk_bf16_f32 v50, v167, v171
	v_cvt_pk_bf16_f32 v51, v175, v179
	v_cvt_pk_bf16_f32 v52, v183, v187
	v_cvt_pk_bf16_f32 v53, v191, v195
	global_store_dwordx4 v43, v[50:53], s[14:15] nt
	v_cvt_pk_bf16_f32 v46, v168, v172
	v_cvt_pk_bf16_f32 v47, v176, v180
	v_cvt_pk_bf16_f32 v48, v184, v188
	v_cvt_pk_bf16_f32 v49, v192, v196
	global_store_dwordx4 v44, v[46:49], s[14:15] nt
	v_cvt_pk_bf16_f32 v50, v169, v173
	v_cvt_pk_bf16_f32 v51, v177, v181
	v_cvt_pk_bf16_f32 v52, v185, v189
	v_cvt_pk_bf16_f32 v53, v193, v197
	global_store_dwordx4 v45, v[50:53], s[14:15] nt
	global_load_dwordx4 v[166:169], v34, s[8:9] offset:2432 nt
	global_load_dwordx4 v[170:173], v35, s[8:9] offset:2432 nt
	global_load_dwordx4 v[174:177], v36, s[8:9] offset:2432 nt
	global_load_dwordx4 v[178:181], v37, s[8:9] offset:2432 nt
	global_load_dwordx4 v[182:185], v38, s[8:9] offset:2432 nt
	global_load_dwordx4 v[186:189], v39, s[8:9] offset:2432 nt
	global_load_dwordx4 v[190:193], v40, s[8:9] offset:2432 nt
	global_load_dwordx4 v[194:197], v41, s[8:9] offset:2432 nt
	s_waitcnt vmcnt(36)
	s_cmp_eq_u32 s25, 0
	s_movk_i32 s6, 0x200
	s_cmovk_i32 s6, 0x400
	s_add_u32 s6, s6, s24
	s_lshl_b32 s6, s6, s26
	s_add_u32 s14, s12, s6
	s_addc_u32 s15, s13, 0
	v_cvt_pk_bf16_f32 v46, v54, v58
	v_cvt_pk_bf16_f32 v47, v62, v66
	v_cvt_pk_bf16_f32 v48, v70, v74
	v_cvt_pk_bf16_f32 v49, v78, v82
	global_store_dwordx4 v42, v[46:49], s[14:15] nt
	v_cvt_pk_bf16_f32 v50, v55, v59
	v_cvt_pk_bf16_f32 v51, v63, v67
	v_cvt_pk_bf16_f32 v52, v71, v75
	v_cvt_pk_bf16_f32 v53, v79, v83
	global_store_dwordx4 v43, v[50:53], s[14:15] nt
	v_cvt_pk_bf16_f32 v46, v56, v60
	v_cvt_pk_bf16_f32 v47, v64, v68
	v_cvt_pk_bf16_f32 v48, v72, v76
	v_cvt_pk_bf16_f32 v49, v80, v84
	global_store_dwordx4 v44, v[46:49], s[14:15] nt
	v_cvt_pk_bf16_f32 v50, v57, v61
	v_cvt_pk_bf16_f32 v51, v65, v69
	v_cvt_pk_bf16_f32 v52, v73, v77
	v_cvt_pk_bf16_f32 v53, v81, v85
	global_store_dwordx4 v45, v[50:53], s[14:15] nt
	global_load_dwordx4 v[54:57], v34, s[8:9] offset:2560 nt
	global_load_dwordx4 v[58:61], v35, s[8:9] offset:2560 nt
	global_load_dwordx4 v[62:65], v36, s[8:9] offset:2560 nt
	global_load_dwordx4 v[66:69], v37, s[8:9] offset:2560 nt
	global_load_dwordx4 v[70:73], v38, s[8:9] offset:2560 nt
	global_load_dwordx4 v[74:77], v39, s[8:9] offset:2560 nt
	global_load_dwordx4 v[78:81], v40, s[8:9] offset:2560 nt
	global_load_dwordx4 v[82:85], v41, s[8:9] offset:2560 nt
	s_waitcnt vmcnt(36)
	s_cmp_eq_u32 s25, 0
	s_movk_i32 s6, 0x220
	s_cmovk_i32 s6, 0x420
	s_add_u32 s6, s6, s24
	s_lshl_b32 s6, s6, s26
	s_add_u32 s14, s12, s6
	s_addc_u32 s15, s13, 0
	v_cvt_pk_bf16_f32 v46, v86, v90
	v_cvt_pk_bf16_f32 v47, v94, v98
	v_cvt_pk_bf16_f32 v48, v102, v106
	v_cvt_pk_bf16_f32 v49, v110, v114
	global_store_dwordx4 v42, v[46:49], s[14:15] nt
	v_cvt_pk_bf16_f32 v50, v87, v91
	v_cvt_pk_bf16_f32 v51, v95, v99
	v_cvt_pk_bf16_f32 v52, v103, v107
	v_cvt_pk_bf16_f32 v53, v111, v115
	global_store_dwordx4 v43, v[50:53], s[14:15] nt
	v_cvt_pk_bf16_f32 v46, v88, v92
	v_cvt_pk_bf16_f32 v47, v96, v100
	v_cvt_pk_bf16_f32 v48, v104, v108
	v_cvt_pk_bf16_f32 v49, v112, v116
	global_store_dwordx4 v44, v[46:49], s[14:15] nt
	v_cvt_pk_bf16_f32 v50, v89, v93
	v_cvt_pk_bf16_f32 v51, v97, v101
	v_cvt_pk_bf16_f32 v52, v105, v109
	v_cvt_pk_bf16_f32 v53, v113, v117
	global_store_dwordx4 v45, v[50:53], s[14:15] nt
	global_load_dwordx4 v[86:89], v34, s[8:9] offset:2688 nt
	global_load_dwordx4 v[90:93], v35, s[8:9] offset:2688 nt
	global_load_dwordx4 v[94:97], v36, s[8:9] offset:2688 nt
	global_load_dwordx4 v[98:101], v37, s[8:9] offset:2688 nt
	global_load_dwordx4 v[102:105], v38, s[8:9] offset:2688 nt
	global_load_dwordx4 v[106:109], v39, s[8:9] offset:2688 nt
	global_load_dwordx4 v[110:113], v40, s[8:9] offset:2688 nt
	global_load_dwordx4 v[114:117], v41, s[8:9] offset:2688 nt
	s_waitcnt vmcnt(36)
	s_cmp_eq_u32 s25, 0
	s_movk_i32 s6, 0x240
	s_cmovk_i32 s6, 0x440
	s_add_u32 s6, s6, s24
	s_lshl_b32 s6, s6, s26
	s_add_u32 s14, s12, s6
	s_addc_u32 s15, s13, 0
	v_cvt_pk_bf16_f32 v46, v118, v122
	v_cvt_pk_bf16_f32 v47, v126, v130
	v_cvt_pk_bf16_f32 v48, v134, v138
	v_cvt_pk_bf16_f32 v49, v142, v146
	global_store_dwordx4 v42, v[46:49], s[14:15] nt
	v_cvt_pk_bf16_f32 v50, v119, v123
	v_cvt_pk_bf16_f32 v51, v127, v131
	v_cvt_pk_bf16_f32 v52, v135, v139
	v_cvt_pk_bf16_f32 v53, v143, v147
	global_store_dwordx4 v43, v[50:53], s[14:15] nt
	v_cvt_pk_bf16_f32 v46, v120, v124
	v_cvt_pk_bf16_f32 v47, v128, v132
	v_cvt_pk_bf16_f32 v48, v136, v140
	v_cvt_pk_bf16_f32 v49, v144, v148
	global_store_dwordx4 v44, v[46:49], s[14:15] nt
	v_cvt_pk_bf16_f32 v50, v121, v125
	v_cvt_pk_bf16_f32 v51, v129, v133
	v_cvt_pk_bf16_f32 v52, v137, v141
	v_cvt_pk_bf16_f32 v53, v145, v149
	global_store_dwordx4 v45, v[50:53], s[14:15] nt
	global_load_dwordx4 v[118:121], v34, s[8:9] offset:2816 nt
	global_load_dwordx4 v[122:125], v35, s[8:9] offset:2816 nt
	global_load_dwordx4 v[126:129], v36, s[8:9] offset:2816 nt
	global_load_dwordx4 v[130:133], v37, s[8:9] offset:2816 nt
	global_load_dwordx4 v[134:137], v38, s[8:9] offset:2816 nt
	global_load_dwordx4 v[138:141], v39, s[8:9] offset:2816 nt
	global_load_dwordx4 v[142:145], v40, s[8:9] offset:2816 nt
	global_load_dwordx4 v[146:149], v41, s[8:9] offset:2816 nt
	s_waitcnt vmcnt(36)
; #define GAS __attribute__((address_space(1)))
; #define LAS __attribute__((address_space(3)))
; #define LDS_WAIT() asm volatile("s_waitcnt lgkmcnt(0)" ::: "memory")
; __device__ __forceinline__ unsigned pk2(float lo, float hi) { unsigned r; asm("v_cvt_pk_bf16_f32 %0, %1, %2" : "=v"(r) : "v"(lo), "v"(hi)); return r; }
; __device__ __forceinline__ void t_load(const TItem& d, f32x4 (&r)[8], int lane) {
;     const float* p = d.W + (size_t)(d.k0 + (lane >> 3)) * d.N + d.n0 + (lane & 7) * 4;
; #pragma unroll
;     for (int i = 0; i < 8; ++i) r[i] = __builtin_nontemporal_load((const f32x4*)(p + (size_t)(8 * i) * d.N));
; }
; __device__ __forceinline__ void t_store(const TItem& d, const f32x4 (&r)[8], LAS float* scr, int lane) {
; #pragma unroll
;     for (int i = 0; i < 8; ++i) *(LAS f32x4*)(scr + (8 * i + (lane >> 3)) * 32 + (((lane & 7) * 4 + 8 * i) & 31)) = r[i];
;     LDS_WAIT(); asm volatile("" ::: "memory");
;     const int c = lane >> 3, nl = lane & 7;
; #pragma unroll
;     for (int j = 0; j < 4; ++j) { const int n = nl + 8 * j; const LAS float* s = scr + (8 * c) * 32 + ((n + 8 * c) & 31);
;         v4u o; o.x = pk2(s[0 * 32], s[1 * 32]); o.y = pk2(s[2 * 32], s[3 * 32]); o.z = pk2(s[4 * 32], s[5 * 32]); o.w = pk2(s[6 * 32], s[7 * 32]);
;         __builtin_nontemporal_store(o, (GAS v4u*)(d.WT + (size_t)t_drow(d.kind, d.n0 + n) * d.K + d.k0 + 8 * c)); }
; __global__ void __launch_bounds__(512, 2) mk_fwd(Params p_unused) {
;     ...
;             for (unsigned tb = grab(); tb < NTICK; tb = grab()) {
;                 TItem a0 = decode((int)(2u * tb)); TItem a1 = a0; a1.n0 += 32;
;                 f32x4 ra[8], rb[8], rc[8], rd[8]; t_load(a0, ra, lane); t_load(a1, rb, lane);
;                 _Pragma("unroll 1") for (unsigned u = 0; u < 8u; u += 2u) {
;                     const TItem b0 = decode((int)(2u * (tb + u + 1u))); TItem b1 = b0; b1.n0 += 32;
;                     t_load(b0, rc, lane); t_load(b1, rd, lane);
;                     t_store(a0, ra, scr, lane); t_store(a1, rb, scr, lane);
;                     if (u + 2u < 8u) { a0 = decode((int)(2u * (tb + u + 2u))); a1 = a0; a1.n0 += 32; t_load(a0, ra, lane); t_load(a1, rb, lane); }
;                     t_store(b0, rc, scr, lane); t_store(b1, rd, scr, lane);
;                 }
	s_cmp_eq_u32 s25, 0
	s_movk_i32 s6, 0x260
	s_cmovk_i32 s6, 0x460
	s_add_u32 s6, s6, s24
	s_lshl_b32 s6, s6, s26
	s_add_u32 s14, s12, s6
	s_addc_u32 s15, s13, 0
	v_cvt_pk_bf16_f32 v46, v166, v170
	v_cvt_pk_bf16_f32 v47, v174, v178
	v_cvt_pk_bf16_f32 v48, v182, v186
	v_cvt_pk_bf16_f32 v49, v190, v194
	global_store_dwordx4 v42, v[46:49], s[14:15] nt
	v_cvt_pk_bf16_f32 v50, v167, v171
	v_cvt_pk_bf16_f32 v51, v175, v179
	v_cvt_pk_bf16_f32 v52, v183, v187
	v_cvt_pk_bf16_f32 v53, v191, v195
	global_store_dwordx4 v43, v[50:53], s[14:15] nt
	v_cvt_pk_bf16_f32 v46, v168, v172
	v_cvt_pk_bf16_f32 v47, v176, v180
	v_cvt_pk_bf16_f32 v48, v184, v188
	v_cvt_pk_bf16_f32 v49, v192, v196
	global_store_dwordx4 v44, v[46:49], s[14:15] nt
	v_cvt_pk_bf16_f32 v50, v169, v173
	v_cvt_pk_bf16_f32 v51, v177, v181
	v_cvt_pk_bf16_f32 v52, v185, v189
	v_cvt_pk_bf16_f32 v53, v193, v197
	global_store_dwordx4 v45, v[50:53], s[14:15] nt
	global_load_dwordx4 v[166:169], v34, s[8:9] offset:2944 nt
	global_load_dwordx4 v[170:173], v35, s[8:9] offset:2944 nt
	global_load_dwordx4 v[174:177], v36, s[8:9] offset:2944 nt
	global_load_dwordx4 v[178:181], v37, s[8:9] offset:2944 nt
	global_load_dwordx4 v[182:185], v38, s[8:9] offset:2944 nt
	global_load_dwordx4 v[186:189], v39, s[8:9] offset:2944 nt
	global_load_dwordx4 v[190:193], v40, s[8:9] offset:2944 nt
	global_load_dwordx4 v[194:197], v41, s[8:9] offset:2944 nt
	s_waitcnt vmcnt(36)
	s_cmp_eq_u32 s25, 0
	s_movk_i32 s6, 0x280
	s_cmovk_i32 s6, 0x500
	s_add_u32 s6, s6, s24
	s_lshl_b32 s6, s6, s26
	s_add_u32 s14, s12, s6
	s_addc_u32 s15, s13, 0
	v_cvt_pk_bf16_f32 v46, v54, v58
	v_cvt_pk_bf16_f32 v47, v62, v66
	v_cvt_pk_bf16_f32 v48, v70, v74
	v_cvt_pk_bf16_f32 v49, v78, v82
	global_store_dwordx4 v42, v[46:49], s[14:15] nt
	v_cvt_pk_bf16_f32 v50, v55, v59
	v_cvt_pk_bf16_f32 v51, v63, v67
	v_cvt_pk_bf16_f32 v52, v71, v75
	v_cvt_pk_bf16_f32 v53, v79, v83
	global_store_dwordx4 v43, v[50:53], s[14:15] nt
	v_cvt_pk_bf16_f32 v46, v56, v60
	v_cvt_pk_bf16_f32 v47, v64, v68
	v_cvt_pk_bf16_f32 v48, v72, v76
	v_cvt_pk_bf16_f32 v49, v80, v84
	global_store_dwordx4 v44, v[46:49], s[14:15] nt
	v_cvt_pk_bf16_f32 v50, v57, v61
	v_cvt_pk_bf16_f32 v51, v65, v69
	v_cvt_pk_bf16_f32 v52, v73, v77
	v_cvt_pk_bf16_f32 v53, v81, v85
	global_store_dwordx4 v45, v[50:53], s[14:15] nt
	global_load_dwordx4 v[54:57], v34, s[8:9] offset:3072 nt
	global_load_dwordx4 v[58:61], v35, s[8:9] offset:3072 nt
	global_load_dwordx4 v[62:65], v36, s[8:9] offset:3072 nt
	global_load_dwordx4 v[66:69], v37, s[8:9] offset:3072 nt
	global_load_dwordx4 v[70:73], v38, s[8:9] offset:3072 nt
	global_load_dwordx4 v[74:77], v39, s[8:9] offset:3072 nt
	global_load_dwordx4 v[78:81], v40, s[8:9] offset:3072 nt
	global_load_dwordx4 v[82:85], v41, s[8:9] offset:3072 nt
	s_waitcnt vmcnt(36)
	s_cmp_eq_u32 s25, 0
	s_movk_i32 s6, 0x2a0
	s_cmovk_i32 s6, 0x520
	s_add_u32 s6, s6, s24
	s_lshl_b32 s6, s6, s26
	s_add_u32 s14, s12, s6
	s_addc_u32 s15, s13, 0
	v_cvt_pk_bf16_f32 v46, v86, v90
	v_cvt_pk_bf16_f32 v47, v94, v98
	v_cvt_pk_bf16_f32 v48, v102, v106
	v_cvt_pk_bf16_f32 v49, v110, v114
	global_store_dwordx4 v42, v[46:49], s[14:15] nt
	v_cvt_pk_bf16_f32 v50, v87, v91
	v_cvt_pk_bf16_f32 v51, v95, v99
	v_cvt_pk_bf16_f32 v52, v103, v107
	v_cvt_pk_bf16_f32 v53, v111, v115
	global_store_dwordx4 v43, v[50:53], s[14:15] nt
	v_cvt_pk_bf16_f32 v46, v88, v92
	v_cvt_pk_bf16_f32 v47, v96, v100
	v_cvt_pk_bf16_f32 v48, v104, v108
	v_cvt_pk_bf16_f32 v49, v112, v116
	global_store_dwordx4 v44, v[46:49], s[14:15] nt
	v_cvt_pk_bf16_f32 v50, v89, v93
	v_cvt_pk_bf16_f32 v51, v97, v101
	v_cvt_pk_bf16_f32 v52, v105, v109
	v_cvt_pk_bf16_f32 v53, v113, v117
	global_store_dwordx4 v45, v[50:53], s[14:15] nt
	global_load_dwordx4 v[86:89], v34, s[8:9] offset:3200 nt
	global_load_dwordx4 v[90:93], v35, s[8:9] offset:3200 nt
	global_load_dwordx4 v[94:97], v36, s[8:9] offset:3200 nt
	global_load_dwordx4 v[98:101], v37, s[8:9] offset:3200 nt
	global_load_dwordx4 v[102:105], v38, s[8:9] offset:3200 nt
	global_load_dwordx4 v[106:109], v39, s[8:9] offset:3200 nt
	global_load_dwordx4 v[110:113], v40, s[8:9] offset:3200 nt
	global_load_dwordx4 v[114:117], v41, s[8:9] offset:3200 nt
	s_waitcnt vmcnt(36)
	s_cmp_eq_u32 s25, 0
	s_movk_i32 s6, 0x2c0
	s_cmovk_i32 s6, 0x540
	s_add_u32 s6, s6, s24
	s_lshl_b32 s6, s6, s26
	s_add_u32 s14, s12, s6
	s_addc_u32 s15, s13, 0
	v_cvt_pk_bf16_f32 v46, v118, v122
	v_cvt_pk_bf16_f32 v47, v126, v130
	v_cvt_pk_bf16_f32 v48, v134, v138
	v_cvt_pk_bf16_f32 v49, v142, v146
	global_store_dwordx4 v42, v[46:49], s[14:15] nt
	v_cvt_pk_bf16_f32 v50, v119, v123
	v_cvt_pk_bf16_f32 v51, v127, v131
	v_cvt_pk_bf16_f32 v52, v135, v139
	v_cvt_pk_bf16_f32 v53, v143, v147
	global_store_dwordx4 v43, v[50:53], s[14:15] nt
	v_cvt_pk_bf16_f32 v46, v120, v124
	v_cvt_pk_bf16_f32 v47, v128, v132
	v_cvt_pk_bf16_f32 v48, v136, v140
	v_cvt_pk_bf16_f32 v49, v144, v148
	global_store_dwordx4 v44, v[46:49], s[14:15] nt
	v_cvt_pk_bf16_f32 v50, v121, v125
	v_cvt_pk_bf16_f32 v51, v129, v133
	v_cvt_pk_bf16_f32 v52, v137, v141
	v_cvt_pk_bf16_f32 v53, v145, v149
	global_store_dwordx4 v45, v[50:53], s[14:15] nt
	global_load_dwordx4 v[118:121], v34, s[8:9] offset:3328 nt
	global_load_dwordx4 v[122:125], v35, s[8:9] offset:3328 nt
	global_load_dwordx4 v[126:129], v36, s[8:9] offset:3328 nt
	global_load_dwordx4 v[130:133], v37, s[8:9] offset:3328 nt
	global_load_dwordx4 v[134:137], v38, s[8:9] offset:3328 nt
	global_load_dwordx4 v[138:141], v39, s[8:9] offset:3328 nt
	global_load_dwordx4 v[142:145], v40, s[8:9] offset:3328 nt
	global_load_dwordx4 v[146:149], v41, s[8:9] offset:3328 nt
	s_waitcnt vmcnt(36)
; #define GAS __attribute__((address_space(1)))
; #define LAS __attribute__((address_space(3)))
; #define LDS_WAIT() asm volatile("s_waitcnt lgkmcnt(0)" ::: "memory")
; __device__ __forceinline__ unsigned pk2(float lo, float hi) { unsigned r; asm("v_cvt_pk_bf16_f32 %0, %1, %2" : "=v"(r) : "v"(lo), "v"(hi)); return r; }
; __device__ __forceinline__ void t_load(const TItem& d, f32x4 (&r)[8], int lane) {
;     const float* p = d.W + (size_t)(d.k0 + (lane >> 3)) * d.N + d.n0 + (lane & 7) * 4;
; #pragma unroll
;     for (int i = 0; i < 8; ++i) r[i] = __builtin_nontemporal_load((const f32x4*)(p + (size_t)(8 * i) * d.N));
; }
; __device__ __forceinline__ void t_store(const TItem& d, const f32x4 (&r)[8], LAS float* scr, int lane) {
; #pragma unroll
;     for (int i = 0; i < 8; ++i) *(LAS f32x4*)(scr + (8 * i + (lane >> 3)) * 32 + (((lane & 7) * 4 + 8 * i) & 31)) = r[i];
;     LDS_WAIT(); asm volatile("" ::: "memory");
;     const int c = lane >> 3, nl = lane & 7;
; #pragma unroll
;     for (int j = 0; j < 4; ++j) { const int n = nl + 8 * j; const LAS float* s = scr + (8 * c) * 32 + ((n + 8 * c) & 31);
;         v4u o; o.x = pk2(s[0 * 32], s[1 * 32]); o.y = pk2(s[2 * 32], s[3 * 32]); o.z = pk2(s[4 * 32], s[5 * 32]); o.w = pk2(s[6 * 32], s[7 * 32]);
;         __builtin_nontemporal_store(o, (GAS v4u*)(d.WT + (size_t)t_drow(d.kind, d.n0 + n) * d.K + d.k0 + 8 * c)); }
; __global__ void __launch_bounds__(512, 2) mk_fwd(Params p_unused) {
;     ...
;             for (unsigned tb = grab(); tb < NTICK; tb = grab()) {
;                 TItem a0 = decode((int)(2u * tb)); TItem a1 = a0; a1.n0 += 32;
;                 f32x4 ra[8], rb[8], rc[8], rd[8]; t_load(a0, ra, lane); t_load(a1, rb, lane);
;                 _Pragma("unroll 1") for (unsigned u = 0; u < 8u; u += 2u) {
;                     const TItem b0 = decode((int)(2u * (tb + u + 1u))); TItem b1 = b0; b1.n0 += 32;
;                     t_load(b0, rc, lane); t_load(b1, rd, lane);
;                     t_store(a0, ra, scr, lane); t_store(a1, rb, scr, lane);
;                     if (u + 2u < 8u) { a0 = decode((int)(2u * (tb + u + 2u))); a1 = a0; a1.n0 += 32; t_load(a0, ra, lane); t_load(a1, rb, lane); }
;                     t_store(b0, rc, scr, lane); t_store(b1, rd, scr, lane);
;                 }
	s_cmp_eq_u32 s25, 0
	s_movk_i32 s6, 0x2e0
	s_cmovk_i32 s6, 0x560
	s_add_u32 s6, s6, s24
	s_lshl_b32 s6, s6, s26
	s_add_u32 s14, s12, s6
	s_addc_u32 s15, s13, 0
	v_cvt_pk_bf16_f32 v46, v166, v170
	v_cvt_pk_bf16_f32 v47, v174, v178
	v_cvt_pk_bf16_f32 v48, v182, v186
	v_cvt_pk_bf16_f32 v49, v190, v194
	global_store_dwordx4 v42, v[46:49], s[14:15] nt
	v_cvt_pk_bf16_f32 v50, v167, v171
	v_cvt_pk_bf16_f32 v51, v175, v179
	v_cvt_pk_bf16_f32 v52, v183, v187
	v_cvt_pk_bf16_f32 v53, v191, v195
	global_store_dwordx4 v43, v[50:53], s[14:15] nt
	v_cvt_pk_bf16_f32 v46, v168, v172
	v_cvt_pk_bf16_f32 v47, v176, v180
	v_cvt_pk_bf16_f32 v48, v184, v188
	v_cvt_pk_bf16_f32 v49, v192, v196
	global_store_dwordx4 v44, v[46:49], s[14:15] nt
	v_cvt_pk_bf16_f32 v50, v169, v173
	v_cvt_pk_bf16_f32 v51, v177, v181
	v_cvt_pk_bf16_f32 v52, v185, v189
	v_cvt_pk_bf16_f32 v53, v193, v197
	global_store_dwordx4 v45, v[50:53], s[14:15] nt
	global_load_dwordx4 v[166:169], v34, s[8:9] offset:3456 nt
	global_load_dwordx4 v[170:173], v35, s[8:9] offset:3456 nt
	global_load_dwordx4 v[174:177], v36, s[8:9] offset:3456 nt
	global_load_dwordx4 v[178:181], v37, s[8:9] offset:3456 nt
	global_load_dwordx4 v[182:185], v38, s[8:9] offset:3456 nt
	global_load_dwordx4 v[186:189], v39, s[8:9] offset:3456 nt
	global_load_dwordx4 v[190:193], v40, s[8:9] offset:3456 nt
	global_load_dwordx4 v[194:197], v41, s[8:9] offset:3456 nt
	s_waitcnt vmcnt(36)
	s_cmp_eq_u32 s25, 0
	s_movk_i32 s6, 0x300
	s_cmovk_i32 s6, 0x600
	s_add_u32 s6, s6, s24
	s_lshl_b32 s6, s6, s26
	s_add_u32 s14, s12, s6
	s_addc_u32 s15, s13, 0
	v_cvt_pk_bf16_f32 v46, v54, v58
	v_cvt_pk_bf16_f32 v47, v62, v66
	v_cvt_pk_bf16_f32 v48, v70, v74
	v_cvt_pk_bf16_f32 v49, v78, v82
	global_store_dwordx4 v42, v[46:49], s[14:15] nt
	v_cvt_pk_bf16_f32 v50, v55, v59
	v_cvt_pk_bf16_f32 v51, v63, v67
	v_cvt_pk_bf16_f32 v52, v71, v75
	v_cvt_pk_bf16_f32 v53, v79, v83
	global_store_dwordx4 v43, v[50:53], s[14:15] nt
	v_cvt_pk_bf16_f32 v46, v56, v60
	v_cvt_pk_bf16_f32 v47, v64, v68
	v_cvt_pk_bf16_f32 v48, v72, v76
	v_cvt_pk_bf16_f32 v49, v80, v84
	global_store_dwordx4 v44, v[46:49], s[14:15] nt
	v_cvt_pk_bf16_f32 v50, v57, v61
	v_cvt_pk_bf16_f32 v51, v65, v69
	v_cvt_pk_bf16_f32 v52, v73, v77
	v_cvt_pk_bf16_f32 v53, v81, v85
	global_store_dwordx4 v45, v[50:53], s[14:15] nt
	global_load_dwordx4 v[54:57], v34, s[8:9] offset:3584 nt
	global_load_dwordx4 v[58:61], v35, s[8:9] offset:3584 nt
	global_load_dwordx4 v[62:65], v36, s[8:9] offset:3584 nt
	global_load_dwordx4 v[66:69], v37, s[8:9] offset:3584 nt
	global_load_dwordx4 v[70:73], v38, s[8:9] offset:3584 nt
	global_load_dwordx4 v[74:77], v39, s[8:9] offset:3584 nt
	global_load_dwordx4 v[78:81], v40, s[8:9] offset:3584 nt
	global_load_dwordx4 v[82:85], v41, s[8:9] offset:3584 nt
	s_waitcnt vmcnt(36)
	s_cmp_eq_u32 s25, 0
	s_movk_i32 s6, 0x320
	s_cmovk_i32 s6, 0x620
	s_add_u32 s6, s6, s24
	s_lshl_b32 s6, s6, s26
	s_add_u32 s14, s12, s6
	s_addc_u32 s15, s13, 0
	v_cvt_pk_bf16_f32 v46, v86, v90
	v_cvt_pk_bf16_f32 v47, v94, v98
	v_cvt_pk_bf16_f32 v48, v102, v106
	v_cvt_pk_bf16_f32 v49, v110, v114
	global_store_dwordx4 v42, v[46:49], s[14:15] nt
	v_cvt_pk_bf16_f32 v50, v87, v91
	v_cvt_pk_bf16_f32 v51, v95, v99
	v_cvt_pk_bf16_f32 v52, v103, v107
	v_cvt_pk_bf16_f32 v53, v111, v115
	global_store_dwordx4 v43, v[50:53], s[14:15] nt
	v_cvt_pk_bf16_f32 v46, v88, v92
	v_cvt_pk_bf16_f32 v47, v96, v100
	v_cvt_pk_bf16_f32 v48, v104, v108
	v_cvt_pk_bf16_f32 v49, v112, v116
	global_store_dwordx4 v44, v[46:49], s[14:15] nt
	v_cvt_pk_bf16_f32 v50, v89, v93
	v_cvt_pk_bf16_f32 v51, v97, v101
	v_cvt_pk_bf16_f32 v52, v105, v109
	v_cvt_pk_bf16_f32 v53, v113, v117
	global_store_dwordx4 v45, v[50:53], s[14:15] nt
	global_load_dwordx4 v[86:89], v34, s[8:9] offset:3712 nt
	global_load_dwordx4 v[90:93], v35, s[8:9] offset:3712 nt
	global_load_dwordx4 v[94:97], v36, s[8:9] offset:3712 nt
	global_load_dwordx4 v[98:101], v37, s[8:9] offset:3712 nt
	global_load_dwordx4 v[102:105], v38, s[8:9] offset:3712 nt
	global_load_dwordx4 v[106:109], v39, s[8:9] offset:3712 nt
	global_load_dwordx4 v[110:113], v40, s[8:9] offset:3712 nt
	global_load_dwordx4 v[114:117], v41, s[8:9] offset:3712 nt
	s_waitcnt vmcnt(36)
	s_cmp_eq_u32 s25, 0
	s_movk_i32 s6, 0x340
	s_cmovk_i32 s6, 0x640
	s_add_u32 s6, s6, s24
	s_lshl_b32 s6, s6, s26
	s_add_u32 s14, s12, s6
	s_addc_u32 s15, s13, 0
	v_cvt_pk_bf16_f32 v46, v118, v122
	v_cvt_pk_bf16_f32 v47, v126, v130
	v_cvt_pk_bf16_f32 v48, v134, v138
	v_cvt_pk_bf16_f32 v49, v142, v146
	global_store_dwordx4 v42, v[46:49], s[14:15] nt
	v_cvt_pk_bf16_f32 v50, v119, v123
	v_cvt_pk_bf16_f32 v51, v127, v131
	v_cvt_pk_bf16_f32 v52, v135, v139
	v_cvt_pk_bf16_f32 v53, v143, v147
	global_store_dwordx4 v43, v[50:53], s[14:15] nt
	v_cvt_pk_bf16_f32 v46, v120, v124
	v_cvt_pk_bf16_f32 v47, v128, v132
	v_cvt_pk_bf16_f32 v48, v136, v140
	v_cvt_pk_bf16_f32 v49, v144, v148
	global_store_dwordx4 v44, v[46:49], s[14:15] nt
	v_cvt_pk_bf16_f32 v50, v121, v125
	v_cvt_pk_bf16_f32 v51, v129, v133
	v_cvt_pk_bf16_f32 v52, v137, v141
	v_cvt_pk_bf16_f32 v53, v145, v149
	global_store_dwordx4 v45, v[50:53], s[14:15] nt
	global_load_dwordx4 v[118:121], v34, s[8:9] offset:3840 nt
	global_load_dwordx4 v[122:125], v35, s[8:9] offset:3840 nt
	global_load_dwordx4 v[126:129], v36, s[8:9] offset:3840 nt
	global_load_dwordx4 v[130:133], v37, s[8:9] offset:3840 nt
	global_load_dwordx4 v[134:137], v38, s[8:9] offset:3840 nt
	global_load_dwordx4 v[138:141], v39, s[8:9] offset:3840 nt
	global_load_dwordx4 v[142:145], v40, s[8:9] offset:3840 nt
	global_load_dwordx4 v[146:149], v41, s[8:9] offset:3840 nt
	s_waitcnt vmcnt(36)
; #define GAS __attribute__((address_space(1)))
; #define LAS __attribute__((address_space(3)))
; #define LDS_WAIT() asm volatile("s_waitcnt lgkmcnt(0)" ::: "memory")
; __device__ __forceinline__ unsigned pk2(float lo, float hi) { unsigned r; asm("v_cvt_pk_bf16_f32 %0, %1, %2" : "=v"(r) : "v"(lo), "v"(hi)); return r; }
; __device__ __forceinline__ void t_load(const TItem& d, f32x4 (&r)[8], int lane) {
;     const float* p = d.W + (size_t)(d.k0 + (lane >> 3)) * d.N + d.n0 + (lane & 7) * 4;
; #pragma unroll
;     for (int i = 0; i < 8; ++i) r[i] = __builtin_nontemporal_load((const f32x4*)(p + (size_t)(8 * i) * d.N));
; }
; __device__ __forceinline__ void t_store(const TItem& d, const f32x4 (&r)[8], LAS float* scr, int lane) {
; #pragma unroll
;     for (int i = 0; i < 8; ++i) *(LAS f32x4*)(scr + (8 * i + (lane >> 3)) * 32 + (((lane & 7) * 4 + 8 * i) & 31)) = r[i];
;     LDS_WAIT(); asm volatile("" ::: "memory");
;     const int c = lane >> 3, nl = lane & 7;
; #pragma unroll
;     for (int j = 0; j < 4; ++j) { const int n = nl + 8 * j; const LAS float* s = scr + (8 * c) * 32 + ((n + 8 * c) & 31);
;         v4u o; o.x = pk2(s[0 * 32], s[1 * 32]); o.y = pk2(s[2 * 32], s[3 * 32]); o.z = pk2(s[4 * 32], s[5 * 32]); o.w = pk2(s[6 * 32], s[7 * 32]);
;         __builtin_nontemporal_store(o, (GAS v4u*)(d.WT + (size_t)t_drow(d.kind, d.n0 + n) * d.K + d.k0 + 8 * c)); }
; __global__ void __launch_bounds__(512, 2) mk_fwd(Params p_unused) {
;     ...
;             for (unsigned tb = grab(); tb < NTICK; tb = grab()) {
;                 TItem a0 = decode((int)(2u * tb)); TItem a1 = a0; a1.n0 += 32;
;                 f32x4 ra[8], rb[8], rc[8], rd[8]; t_load(a0, ra, lane); t_load(a1, rb, lane);
;                 _Pragma("unroll 1") for (unsigned u = 0; u < 8u; u += 2u) {
;                     const TItem b0 = decode((int)(2u * (tb + u + 1u))); TItem b1 = b0; b1.n0 += 32;
;                     t_load(b0, rc, lane); t_load(b1, rd, lane);
;                     t_store(a0, ra, scr, lane); t_store(a1, rb, scr, lane);
;                     if (u + 2u < 8u) { a0 = decode((int)(2u * (tb + u + 2u))); a1 = a0; a1.n0 += 32; t_load(a0, ra, lane); t_load(a1, rb, lane); }
;                     t_store(b0, rc, scr, lane); t_store(b1, rd, scr, lane);
;                 }
	s_cmp_eq_u32 s25, 0
	s_movk_i32 s6, 0x360
	s_cmovk_i32 s6, 0x660
	s_add_u32 s6, s6, s24
	s_lshl_b32 s6, s6, s26
	s_add_u32 s14, s12, s6
	s_addc_u32 s15, s13, 0
	v_cvt_pk_bf16_f32 v46, v166, v170
	v_cvt_pk_bf16_f32 v47, v174, v178
	v_cvt_pk_bf16_f32 v48, v182, v186
	v_cvt_pk_bf16_f32 v49, v190, v194
	global_store_dwordx4 v42, v[46:49], s[14:15] nt
	v_cvt_pk_bf16_f32 v50, v167, v171
	v_cvt_pk_bf16_f32 v51, v175, v179
	v_cvt_pk_bf16_f32 v52, v183, v187
	v_cvt_pk_bf16_f32 v53, v191, v195
	global_store_dwordx4 v43, v[50:53], s[14:15] nt
	v_cvt_pk_bf16_f32 v46, v168, v172
	v_cvt_pk_bf16_f32 v47, v176, v180
	v_cvt_pk_bf16_f32 v48, v184, v188
	v_cvt_pk_bf16_f32 v49, v192, v196
	global_store_dwordx4 v44, v[46:49], s[14:15] nt
	v_cvt_pk_bf16_f32 v50, v169, v173
	v_cvt_pk_bf16_f32 v51, v177, v181
	v_cvt_pk_bf16_f32 v52, v185, v189
	v_cvt_pk_bf16_f32 v53, v193, v197
	global_store_dwordx4 v45, v[50:53], s[14:15] nt
	global_load_dwordx4 v[166:169], v34, s[8:9] offset:3968 nt
	global_load_dwordx4 v[170:173], v35, s[8:9] offset:3968 nt
	global_load_dwordx4 v[174:177], v36, s[8:9] offset:3968 nt
	global_load_dwordx4 v[178:181], v37, s[8:9] offset:3968 nt
	global_load_dwordx4 v[182:185], v38, s[8:9] offset:3968 nt
	global_load_dwordx4 v[186:189], v39, s[8:9] offset:3968 nt
	global_load_dwordx4 v[190:193], v40, s[8:9] offset:3968 nt
	global_load_dwordx4 v[194:197], v41, s[8:9] offset:3968 nt
	s_waitcnt vmcnt(36)
	s_cmp_eq_u32 s25, 0
	s_movk_i32 s6, 0x380
	s_cmovk_i32 s6, 0x700
	s_add_u32 s6, s6, s24
	s_lshl_b32 s6, s6, s26
	s_add_u32 s14, s12, s6
	s_addc_u32 s15, s13, 0
	v_cvt_pk_bf16_f32 v46, v54, v58
	v_cvt_pk_bf16_f32 v47, v62, v66
	v_cvt_pk_bf16_f32 v48, v70, v74
	v_cvt_pk_bf16_f32 v49, v78, v82
	global_store_dwordx4 v42, v[46:49], s[14:15] nt
	v_cvt_pk_bf16_f32 v50, v55, v59
	v_cvt_pk_bf16_f32 v51, v63, v67
	v_cvt_pk_bf16_f32 v52, v71, v75
	v_cvt_pk_bf16_f32 v53, v79, v83
	global_store_dwordx4 v43, v[50:53], s[14:15] nt
	v_cvt_pk_bf16_f32 v46, v56, v60
	v_cvt_pk_bf16_f32 v47, v64, v68
	v_cvt_pk_bf16_f32 v48, v72, v76
	v_cvt_pk_bf16_f32 v49, v80, v84
	global_store_dwordx4 v44, v[46:49], s[14:15] nt
	v_cvt_pk_bf16_f32 v50, v57, v61
	v_cvt_pk_bf16_f32 v51, v65, v69
	v_cvt_pk_bf16_f32 v52, v73, v77
	v_cvt_pk_bf16_f32 v53, v81, v85
	global_store_dwordx4 v45, v[50:53], s[14:15] nt
	s_waitcnt vmcnt(28)
	s_cmp_eq_u32 s25, 0
	s_movk_i32 s6, 0x3a0
	s_cmovk_i32 s6, 0x720
	s_add_u32 s6, s6, s24
	s_lshl_b32 s6, s6, s26
	s_add_u32 s14, s12, s6
	s_addc_u32 s15, s13, 0
	v_cvt_pk_bf16_f32 v46, v86, v90
	v_cvt_pk_bf16_f32 v47, v94, v98
	v_cvt_pk_bf16_f32 v48, v102, v106
	v_cvt_pk_bf16_f32 v49, v110, v114
	global_store_dwordx4 v42, v[46:49], s[14:15] nt
	v_cvt_pk_bf16_f32 v50, v87, v91
	v_cvt_pk_bf16_f32 v51, v95, v99
	v_cvt_pk_bf16_f32 v52, v103, v107
	v_cvt_pk_bf16_f32 v53, v111, v115
	global_store_dwordx4 v43, v[50:53], s[14:15] nt
	v_cvt_pk_bf16_f32 v46, v88, v92
	v_cvt_pk_bf16_f32 v47, v96, v100
	v_cvt_pk_bf16_f32 v48, v104, v108
	v_cvt_pk_bf16_f32 v49, v112, v116
	global_store_dwordx4 v44, v[46:49], s[14:15] nt
	v_cvt_pk_bf16_f32 v50, v89, v93
	v_cvt_pk_bf16_f32 v51, v97, v101
	v_cvt_pk_bf16_f32 v52, v105, v109
	v_cvt_pk_bf16_f32 v53, v113, v117
	global_store_dwordx4 v45, v[50:53], s[14:15] nt
	s_waitcnt vmcnt(20)
	s_cmp_eq_u32 s25, 0
	s_movk_i32 s6, 0x3c0
	s_cmovk_i32 s6, 0x740
	s_add_u32 s6, s6, s24
	s_lshl_b32 s6, s6, s26
	s_add_u32 s14, s12, s6
	s_addc_u32 s15, s13, 0
	v_cvt_pk_bf16_f32 v46, v118, v122
	v_cvt_pk_bf16_f32 v47, v126, v130
	v_cvt_pk_bf16_f32 v48, v134, v138
	v_cvt_pk_bf16_f32 v49, v142, v146
	global_store_dwordx4 v42, v[46:49], s[14:15] nt
	v_cvt_pk_bf16_f32 v50, v119, v123
	v_cvt_pk_bf16_f32 v51, v127, v131
	v_cvt_pk_bf16_f32 v52, v135, v139
	v_cvt_pk_bf16_f32 v53, v143, v147
	global_store_dwordx4 v43, v[50:53], s[14:15] nt
	v_cvt_pk_bf16_f32 v46, v120, v124
	v_cvt_pk_bf16_f32 v47, v128, v132
	v_cvt_pk_bf16_f32 v48, v136, v140
	v_cvt_pk_bf16_f32 v49, v144, v148
	global_store_dwordx4 v44, v[46:49], s[14:15] nt
	v_cvt_pk_bf16_f32 v50, v121, v125
	v_cvt_pk_bf16_f32 v51, v129, v133
	v_cvt_pk_bf16_f32 v52, v137, v141
	v_cvt_pk_bf16_f32 v53, v145, v149
	global_store_dwordx4 v45, v[50:53], s[14:15] nt
	s_waitcnt vmcnt(12)
	s_cmp_eq_u32 s25, 0
	s_movk_i32 s6, 0x3e0
	s_cmovk_i32 s6, 0x760
	s_add_u32 s6, s6, s24
	s_lshl_b32 s6, s6, s26
	s_add_u32 s14, s12, s6
	s_addc_u32 s15, s13, 0
	v_cvt_pk_bf16_f32 v46, v166, v170
	v_cvt_pk_bf16_f32 v47, v174, v178
	v_cvt_pk_bf16_f32 v48, v182, v186
	v_cvt_pk_bf16_f32 v49, v190, v194
	global_store_dwordx4 v42, v[46:49], s[14:15] nt
	v_cvt_pk_bf16_f32 v50, v167, v171
	v_cvt_pk_bf16_f32 v51, v175, v179
	v_cvt_pk_bf16_f32 v52, v183, v187
	v_cvt_pk_bf16_f32 v53, v191, v195
	global_store_dwordx4 v43, v[50:53], s[14:15] nt
	v_cvt_pk_bf16_f32 v46, v168, v172
	v_cvt_pk_bf16_f32 v47, v176, v180
	v_cvt_pk_bf16_f32 v48, v184, v188
	v_cvt_pk_bf16_f32 v49, v192, v196
	global_store_dwordx4 v44, v[46:49], s[14:15] nt
	v_cvt_pk_bf16_f32 v50, v169, v173
	v_cvt_pk_bf16_f32 v51, v177, v181
	v_cvt_pk_bf16_f32 v52, v185, v189
	v_cvt_pk_bf16_f32 v53, v193, v197
	global_store_dwordx4 v45, v[50:53], s[14:15] nt
	v_readfirstlane_b32 s40, v7
	s_nop 3
	s_branch .Lcv_loop
